# GEMM loops: the s_setprio 0 / s_setprio 1 pair between the two 16-MFMA groups of a phase removed (priority stays raised through the 32 MFMAs)
# baseline (speedup 1.0000x reference)
.LBB0_477:
	s_add_u32 s2, s34, 0x80
	s_addc_u32 s3, s35, 0
	s_cmp_eq_u32 s45, 28
	s_cselect_b32 s39, s6, s3
	s_cselect_b32 s38, s7, s2
	s_cselect_b32 s37, s40, s43
	s_cselect_b32 s36, s41, s42
	s_add_i32 s2, 0, 0x10000
	v_add_u32_e32 v2, s2, v180
	s_add_i32 s46, 0, 0x14000
	ds_read_b128 v[148:151], v2
	s_waitcnt lgkmcnt(0)
	ds_read_b128 v[152:155], v2 offset:1024
	ds_read_b128 v[156:159], v2 offset:2048
	ds_read_b128 v[160:163], v2 offset:3072
	v_add_u32_e32 v2, s46, v180
	ds_read_b128 v[164:167], v2
	ds_read_b128 v[168:171], v2 offset:1024
	ds_read_b128 v[172:175], v2 offset:2048
	ds_read_b128 v[182:185], v2 offset:3072
	v_lshl_add_u64 v[176:177], s[34:35], 0, v[146:147]
	s_add_i32 m0, s16, 0xc000
	ds_read_b128 v[190:193], v181
	ds_read_b128 v[212:215], v181 offset:1024
	ds_read_b128 v[216:219], v181 offset:2048
	ds_read_b128 v[224:227], v181 offset:3072
	ds_read_b128 v[228:231], v181 offset:4096
	ds_read_b128 v[232:235], v181 offset:5120
	ds_read_b128 v[236:239], v181 offset:6144
	ds_read_b128 v[240:243], v181 offset:7168
	global_load_lds_dwordx4 v[176:177], off
	v_lshl_add_u64 v[176:177], s[34:35], 0, v[144:145]
	s_add_i32 m0, s16, 0xe000
	s_nop 0
	global_load_lds_dwordx4 v[176:177], off
	s_waitcnt vmcnt(8)
	s_waitcnt lgkmcnt(0)
	s_barrier
	s_setprio 1
	s_waitcnt lgkmcnt(0)
	v_mfma_f32_16x16x32_bf16 v[128:131], v[148:151], v[190:193], v[128:131]
	v_mfma_f32_16x16x32_bf16 v[124:127], v[156:159], v[190:193], v[124:127]
	v_mfma_f32_16x16x32_bf16 v[112:115], v[148:151], v[216:219], v[112:115]
	v_mfma_f32_16x16x32_bf16 v[108:111], v[156:159], v[216:219], v[108:111]
	v_mfma_f32_16x16x32_bf16 v[96:99], v[148:151], v[228:231], v[96:99]
	v_mfma_f32_16x16x32_bf16 v[92:95], v[156:159], v[228:231], v[92:95]
	v_mfma_f32_16x16x32_bf16 v[80:83], v[148:151], v[236:239], v[80:83]
	v_mfma_f32_16x16x32_bf16 v[76:79], v[156:159], v[236:239], v[76:79]
	v_mfma_f32_16x16x32_bf16 v[128:131], v[152:155], v[212:215], v[128:131]
	v_mfma_f32_16x16x32_bf16 v[124:127], v[160:163], v[212:215], v[124:127]
	v_mfma_f32_16x16x32_bf16 v[112:115], v[152:155], v[224:227], v[112:115]
	v_mfma_f32_16x16x32_bf16 v[108:111], v[160:163], v[224:227], v[108:111]
	v_mfma_f32_16x16x32_bf16 v[96:99], v[152:155], v[232:235], v[96:99]
	v_mfma_f32_16x16x32_bf16 v[92:95], v[160:163], v[232:235], v[92:95]
	v_mfma_f32_16x16x32_bf16 v[80:83], v[152:155], v[240:243], v[80:83]
	v_mfma_f32_16x16x32_bf16 v[76:79], v[160:163], v[240:243], v[76:79]
	v_mfma_f32_16x16x32_bf16 v[120:123], v[164:167], v[190:193], v[120:123]
	v_mfma_f32_16x16x32_bf16 v[116:119], v[172:175], v[190:193], v[116:119]
	v_mfma_f32_16x16x32_bf16 v[104:107], v[164:167], v[216:219], v[104:107]
	v_mfma_f32_16x16x32_bf16 v[100:103], v[172:175], v[216:219], v[100:103]
	v_mfma_f32_16x16x32_bf16 v[88:91], v[164:167], v[228:231], v[88:91]
	v_mfma_f32_16x16x32_bf16 v[84:87], v[172:175], v[228:231], v[84:87]
	v_mfma_f32_16x16x32_bf16 v[72:75], v[164:167], v[236:239], v[72:75]
	v_mfma_f32_16x16x32_bf16 v[68:71], v[172:175], v[236:239], v[68:71]
	v_mfma_f32_16x16x32_bf16 v[120:123], v[168:171], v[212:215], v[120:123]
	v_mfma_f32_16x16x32_bf16 v[116:119], v[182:185], v[212:215], v[116:119]
	v_mfma_f32_16x16x32_bf16 v[104:107], v[168:171], v[224:227], v[104:107]
	v_mfma_f32_16x16x32_bf16 v[100:103], v[182:185], v[224:227], v[100:103]
	v_mfma_f32_16x16x32_bf16 v[88:91], v[168:171], v[232:235], v[88:91]
	v_mfma_f32_16x16x32_bf16 v[84:87], v[182:185], v[232:235], v[84:87]
	v_mfma_f32_16x16x32_bf16 v[72:75], v[168:171], v[240:243], v[72:75]
	v_mfma_f32_16x16x32_bf16 v[68:71], v[182:185], v[240:243], v[68:71]
	s_setprio 0
	s_barrier
	s_add_i32 s2, s2, s15
	v_lshl_add_u64 v[176:177], s[36:37], 0, v[132:133]
	s_mov_b32 m0, s2
	ds_read_b128 v[190:193], v181 offset:16384
	ds_read_b128 v[212:215], v181 offset:17408
	ds_read_b128 v[216:219], v181 offset:18432
	ds_read_b128 v[224:227], v181 offset:19456
	ds_read_b128 v[228:231], v181 offset:20480
	ds_read_b128 v[232:235], v181 offset:21504
	ds_read_b128 v[236:239], v181 offset:22528
	ds_read_b128 v[240:243], v181 offset:23552
	global_load_lds_dwordx4 v[176:177], off
	s_add_i32 m0, s2, 0x2000
	s_add_u32 s2, s36, 0x80000
	v_lshl_add_u64 v[186:187], s[36:37], 0, v[134:135]
	s_addc_u32 s3, s37, 0
	s_add_i32 s46, s46, s15
	global_load_lds_dwordx4 v[186:187], off
	v_lshl_add_u64 v[194:195], s[2:3], 0, v[132:133]
	s_mov_b32 m0, s46
	v_lshl_add_u64 v[244:245], s[38:39], 0, v[138:139]
	global_load_lds_dwordx4 v[194:195], off
	v_lshl_add_u64 v[194:195], s[2:3], 0, v[134:135]
	s_add_i32 m0, s46, 0x2000
	s_nop 0
	global_load_lds_dwordx4 v[194:195], off
	v_lshl_add_u64 v[194:195], s[38:39], 0, v[136:137]
	s_mov_b32 m0, s16
	s_nop 0
	global_load_lds_dwordx4 v[194:195], off
	s_mov_b32 m0, s17
	s_nop 0
	global_load_lds_dwordx4 v[244:245], off
	s_waitcnt vmcnt(8)
	s_waitcnt lgkmcnt(0)
	s_barrier
	s_setprio 1
	s_waitcnt lgkmcnt(0)
	v_mfma_f32_16x16x32_bf16 v[64:67], v[148:151], v[190:193], v[64:67]
	v_mfma_f32_16x16x32_bf16 v[60:63], v[156:159], v[190:193], v[60:63]
	v_mfma_f32_16x16x32_bf16 v[48:51], v[148:151], v[216:219], v[48:51]
	v_mfma_f32_16x16x32_bf16 v[44:47], v[156:159], v[216:219], v[44:47]
	v_mfma_f32_16x16x32_bf16 v[32:35], v[148:151], v[228:231], v[32:35]
	v_mfma_f32_16x16x32_bf16 v[28:31], v[156:159], v[228:231], v[28:31]
	v_mfma_f32_16x16x32_bf16 v[16:19], v[148:151], v[236:239], v[16:19]
	v_mfma_f32_16x16x32_bf16 v[4:7], v[156:159], v[236:239], v[4:7]
	v_mfma_f32_16x16x32_bf16 v[64:67], v[152:155], v[212:215], v[64:67]
	v_mfma_f32_16x16x32_bf16 v[60:63], v[160:163], v[212:215], v[60:63]
	v_mfma_f32_16x16x32_bf16 v[48:51], v[152:155], v[224:227], v[48:51]
	v_mfma_f32_16x16x32_bf16 v[44:47], v[160:163], v[224:227], v[44:47]
	v_mfma_f32_16x16x32_bf16 v[32:35], v[152:155], v[232:235], v[32:35]
	v_mfma_f32_16x16x32_bf16 v[28:31], v[160:163], v[232:235], v[28:31]
	v_mfma_f32_16x16x32_bf16 v[16:19], v[152:155], v[240:243], v[16:19]
	v_mfma_f32_16x16x32_bf16 v[4:7], v[160:163], v[240:243], v[4:7]
	v_mfma_f32_16x16x32_bf16 v[52:55], v[164:167], v[190:193], v[52:55]
	v_mfma_f32_16x16x32_bf16 v[56:59], v[172:175], v[190:193], v[56:59]
	v_mfma_f32_16x16x32_bf16 v[36:39], v[164:167], v[216:219], v[36:39]
	v_mfma_f32_16x16x32_bf16 v[40:43], v[172:175], v[216:219], v[40:43]
	v_mfma_f32_16x16x32_bf16 v[20:23], v[164:167], v[228:231], v[20:23]
	v_mfma_f32_16x16x32_bf16 v[24:27], v[172:175], v[228:231], v[24:27]
	v_mfma_f32_16x16x32_bf16 v[8:11], v[164:167], v[236:239], v[8:11]
	v_mfma_f32_16x16x32_bf16 v[12:15], v[172:175], v[236:239], v[12:15]
	v_mfma_f32_16x16x32_bf16 v[52:55], v[168:171], v[212:215], v[52:55]
	v_mfma_f32_16x16x32_bf16 v[56:59], v[182:185], v[212:215], v[56:59]
	v_mfma_f32_16x16x32_bf16 v[36:39], v[168:171], v[224:227], v[36:39]
	v_mfma_f32_16x16x32_bf16 v[40:43], v[182:185], v[224:227], v[40:43]
	v_mfma_f32_16x16x32_bf16 v[20:23], v[168:171], v[232:235], v[20:23]
	v_mfma_f32_16x16x32_bf16 v[24:27], v[182:185], v[232:235], v[24:27]
	v_mfma_f32_16x16x32_bf16 v[8:11], v[168:171], v[240:243], v[8:11]
	v_mfma_f32_16x16x32_bf16 v[12:15], v[182:185], v[240:243], v[12:15]
	s_setprio 0
	s_barrier
	s_add_i32 s2, 0, 0x18000
	v_add_u32_e32 v2, s2, v180
	s_add_i32 s46, 0, 0x1c000
	ds_read_b128 v[148:151], v2
	ds_read_b128 v[152:155], v2 offset:1024
	ds_read_b128 v[156:159], v2 offset:2048
	ds_read_b128 v[160:163], v2 offset:3072
	v_add_u32_e32 v2, s46, v180
	ds_read_b128 v[164:167], v2
	ds_read_b128 v[168:171], v2 offset:1024
	ds_read_b128 v[172:175], v2 offset:2048
	ds_read_b128 v[182:185], v2 offset:3072
	s_mov_b32 m0, s18
	v_lshl_add_u64 v[246:247], s[38:39], 0, v[140:141]
	ds_read_b128 v[190:193], v181 offset:32768
	ds_read_b128 v[212:215], v181 offset:33792
	ds_read_b128 v[216:219], v181 offset:34816
	ds_read_b128 v[224:227], v181 offset:35840
	ds_read_b128 v[228:231], v181 offset:36864
	ds_read_b128 v[232:235], v181 offset:37888
	ds_read_b128 v[236:239], v181 offset:38912
	ds_read_b128 v[240:243], v181 offset:39936
	global_load_lds_dwordx4 v[246:247], off
	v_lshl_add_u64 v[246:247], s[38:39], 0, v[142:143]
	s_mov_b32 m0, s19
	s_nop 0
	global_load_lds_dwordx4 v[246:247], off
	s_waitcnt vmcnt(8)
	s_waitcnt lgkmcnt(0)
	s_barrier
	s_setprio 1
	s_waitcnt lgkmcnt(0)
	v_mfma_f32_16x16x32_bf16 v[128:131], v[148:151], v[190:193], v[128:131]
	v_mfma_f32_16x16x32_bf16 v[124:127], v[156:159], v[190:193], v[124:127]
	v_mfma_f32_16x16x32_bf16 v[112:115], v[148:151], v[216:219], v[112:115]
	v_mfma_f32_16x16x32_bf16 v[108:111], v[156:159], v[216:219], v[108:111]
	v_mfma_f32_16x16x32_bf16 v[96:99], v[148:151], v[228:231], v[96:99]
	v_mfma_f32_16x16x32_bf16 v[92:95], v[156:159], v[228:231], v[92:95]
	v_mfma_f32_16x16x32_bf16 v[80:83], v[148:151], v[236:239], v[80:83]
	v_mfma_f32_16x16x32_bf16 v[76:79], v[156:159], v[236:239], v[76:79]
	v_mfma_f32_16x16x32_bf16 v[128:131], v[152:155], v[212:215], v[128:131]
	v_mfma_f32_16x16x32_bf16 v[124:127], v[160:163], v[212:215], v[124:127]
	v_mfma_f32_16x16x32_bf16 v[112:115], v[152:155], v[224:227], v[112:115]
	v_mfma_f32_16x16x32_bf16 v[108:111], v[160:163], v[224:227], v[108:111]
	v_mfma_f32_16x16x32_bf16 v[96:99], v[152:155], v[232:235], v[96:99]
	v_mfma_f32_16x16x32_bf16 v[92:95], v[160:163], v[232:235], v[92:95]
	v_mfma_f32_16x16x32_bf16 v[80:83], v[152:155], v[240:243], v[80:83]
	v_mfma_f32_16x16x32_bf16 v[76:79], v[160:163], v[240:243], v[76:79]
	v_mfma_f32_16x16x32_bf16 v[120:123], v[164:167], v[190:193], v[120:123]
	v_mfma_f32_16x16x32_bf16 v[116:119], v[172:175], v[190:193], v[116:119]
	v_mfma_f32_16x16x32_bf16 v[104:107], v[164:167], v[216:219], v[104:107]
	v_mfma_f32_16x16x32_bf16 v[100:103], v[172:175], v[216:219], v[100:103]
	v_mfma_f32_16x16x32_bf16 v[88:91], v[164:167], v[228:231], v[88:91]
	v_mfma_f32_16x16x32_bf16 v[84:87], v[172:175], v[228:231], v[84:87]
	v_mfma_f32_16x16x32_bf16 v[72:75], v[164:167], v[236:239], v[72:75]
	v_mfma_f32_16x16x32_bf16 v[68:71], v[172:175], v[236:239], v[68:71]
	v_mfma_f32_16x16x32_bf16 v[120:123], v[168:171], v[212:215], v[120:123]
	v_mfma_f32_16x16x32_bf16 v[116:119], v[182:185], v[212:215], v[116:119]
	v_mfma_f32_16x16x32_bf16 v[104:107], v[168:171], v[224:227], v[104:107]
	v_mfma_f32_16x16x32_bf16 v[100:103], v[182:185], v[224:227], v[100:103]
	v_mfma_f32_16x16x32_bf16 v[88:91], v[168:171], v[232:235], v[88:91]
	v_mfma_f32_16x16x32_bf16 v[84:87], v[182:185], v[232:235], v[84:87]
	v_mfma_f32_16x16x32_bf16 v[72:75], v[168:171], v[240:243], v[72:75]
	v_mfma_f32_16x16x32_bf16 v[68:71], v[182:185], v[240:243], v[68:71]
	s_setprio 0
	s_barrier
	s_add_i32 s2, s2, s15
	v_lshl_add_u64 v[176:177], v[176:177], 0, s[30:31]
	s_mov_b32 m0, s2
	ds_read_b128 v[190:193], v181 offset:49152
	ds_read_b128 v[212:215], v181 offset:50176
	ds_read_b128 v[216:219], v181 offset:51200
	ds_read_b128 v[224:227], v181 offset:52224
	ds_read_b128 v[228:231], v181 offset:53248
	ds_read_b128 v[232:235], v181 offset:54272
	ds_read_b128 v[236:239], v181 offset:55296
	ds_read_b128 v[240:243], v181 offset:56320
	global_load_lds_dwordx4 v[176:177], off
	s_add_i32 m0, s2, 0x2000
	s_add_u32 s2, s36, 0x80080
	v_lshl_add_u64 v[176:177], v[186:187], 0, s[30:31]
	s_addc_u32 s3, s37, 0
	s_add_i32 s36, s46, s15
	global_load_lds_dwordx4 v[176:177], off
	v_lshl_add_u64 v[176:177], s[2:3], 0, v[132:133]
	s_mov_b32 m0, s36
	s_nop 0
	global_load_lds_dwordx4 v[176:177], off
	v_lshl_add_u64 v[176:177], s[2:3], 0, v[134:135]
	s_add_i32 m0, s36, 0x2000
	s_nop 0
	global_load_lds_dwordx4 v[176:177], off
	v_lshl_add_u64 v[176:177], v[194:195], 0, s[30:31]
	s_mov_b32 m0, s22
	s_nop 0
	global_load_lds_dwordx4 v[176:177], off
	v_lshl_add_u64 v[176:177], v[244:245], 0, s[30:31]
	s_mov_b32 m0, s23
	s_nop 0
	global_load_lds_dwordx4 v[176:177], off
	s_waitcnt vmcnt(8)
	s_waitcnt lgkmcnt(0)
	s_barrier
	s_setprio 1
	s_waitcnt lgkmcnt(0)
	v_mfma_f32_16x16x32_bf16 v[64:67], v[148:151], v[190:193], v[64:67]
	v_mfma_f32_16x16x32_bf16 v[60:63], v[156:159], v[190:193], v[60:63]
	v_mfma_f32_16x16x32_bf16 v[48:51], v[148:151], v[216:219], v[48:51]
	v_mfma_f32_16x16x32_bf16 v[44:47], v[156:159], v[216:219], v[44:47]
	v_mfma_f32_16x16x32_bf16 v[32:35], v[148:151], v[228:231], v[32:35]
	v_mfma_f32_16x16x32_bf16 v[28:31], v[156:159], v[228:231], v[28:31]
	v_mfma_f32_16x16x32_bf16 v[16:19], v[148:151], v[236:239], v[16:19]
	v_mfma_f32_16x16x32_bf16 v[4:7], v[156:159], v[236:239], v[4:7]
	v_mfma_f32_16x16x32_bf16 v[64:67], v[152:155], v[212:215], v[64:67]
	v_mfma_f32_16x16x32_bf16 v[60:63], v[160:163], v[212:215], v[60:63]
	v_mfma_f32_16x16x32_bf16 v[48:51], v[152:155], v[224:227], v[48:51]
	v_mfma_f32_16x16x32_bf16 v[44:47], v[160:163], v[224:227], v[44:47]
	v_mfma_f32_16x16x32_bf16 v[32:35], v[152:155], v[232:235], v[32:35]
	v_mfma_f32_16x16x32_bf16 v[28:31], v[160:163], v[232:235], v[28:31]
	v_mfma_f32_16x16x32_bf16 v[16:19], v[152:155], v[240:243], v[16:19]
	v_mfma_f32_16x16x32_bf16 v[4:7], v[160:163], v[240:243], v[4:7]
	v_mfma_f32_16x16x32_bf16 v[52:55], v[164:167], v[190:193], v[52:55]
	v_mfma_f32_16x16x32_bf16 v[56:59], v[172:175], v[190:193], v[56:59]
	v_mfma_f32_16x16x32_bf16 v[36:39], v[164:167], v[216:219], v[36:39]
	v_mfma_f32_16x16x32_bf16 v[40:43], v[172:175], v[216:219], v[40:43]
	v_mfma_f32_16x16x32_bf16 v[20:23], v[164:167], v[228:231], v[20:23]
	v_mfma_f32_16x16x32_bf16 v[24:27], v[172:175], v[228:231], v[24:27]
	v_mfma_f32_16x16x32_bf16 v[8:11], v[164:167], v[236:239], v[8:11]
	v_mfma_f32_16x16x32_bf16 v[12:15], v[172:175], v[236:239], v[12:15]
	v_mfma_f32_16x16x32_bf16 v[52:55], v[168:171], v[212:215], v[52:55]
	v_mfma_f32_16x16x32_bf16 v[56:59], v[182:185], v[212:215], v[56:59]
	v_mfma_f32_16x16x32_bf16 v[36:39], v[168:171], v[224:227], v[36:39]
	v_mfma_f32_16x16x32_bf16 v[40:43], v[182:185], v[224:227], v[40:43]
	v_mfma_f32_16x16x32_bf16 v[20:23], v[168:171], v[232:235], v[20:23]
	v_mfma_f32_16x16x32_bf16 v[24:27], v[182:185], v[232:235], v[24:27]
	v_mfma_f32_16x16x32_bf16 v[8:11], v[168:171], v[240:243], v[8:11]
	v_mfma_f32_16x16x32_bf16 v[12:15], v[182:185], v[240:243], v[12:15]
	s_setprio 0
	s_barrier
	s_add_i32 s45, s45, 2
	s_add_u32 s34, s34, 0x100
	s_addc_u32 s35, s35, 0
	s_add_u32 s42, s42, 0x100
	s_addc_u32 s43, s43, 0
	s_cmp_gt_u32 s45, 29
	s_cbranch_scc0 .LBB0_477
	s_and_b64 vcc, exec, s[76:77]
	s_cbranch_vccz .LBB0_480
	s_barrier

.LBB0_991:
	s_add_u32 s2, s0, 0x80
	s_addc_u32 s3, s1, 0
	s_cmp_eq_u32 s57, 4
	s_cselect_b32 s37, s53, s3
	s_cselect_b32 s36, s52, s2
	s_cselect_b32 s35, s55, s56
	s_cselect_b32 s34, s54, s29
	s_add_i32 s2, 0, 0x10000
	v_add_u32_e32 v2, s2, v168
	s_add_i32 s58, 0, 0x14000
	ds_read_b128 v[148:151], v2
	ds_read_b128 v[152:155], v2 offset:1024
	ds_read_b128 v[156:159], v2 offset:2048
	ds_read_b128 v[160:163], v2 offset:3072
	v_add_u32_e32 v2, s58, v168
	ds_read_b128 v[170:173], v2
	ds_read_b128 v[174:177], v2 offset:1024
	ds_read_b128 v[178:181], v2 offset:2048
	ds_read_b128 v[182:185], v2 offset:3072
	v_lshl_add_u64 v[164:165], s[0:1], 0, v[144:145]
	s_add_i32 m0, s18, 0xc000
	ds_read_b128 v[190:193], v169
	ds_read_b128 v[212:215], v169 offset:1024
	ds_read_b128 v[216:219], v169 offset:2048
	ds_read_b128 v[224:227], v169 offset:3072
	ds_read_b128 v[228:231], v169 offset:4096
	ds_read_b128 v[232:235], v169 offset:5120
	ds_read_b128 v[236:239], v169 offset:6144
	ds_read_b128 v[240:243], v169 offset:7168
	global_load_lds_dwordx4 v[164:165], off
	v_lshl_add_u64 v[164:165], s[0:1], 0, v[146:147]
	s_add_i32 m0, s18, 0xe000
	s_nop 0
	global_load_lds_dwordx4 v[164:165], off
	s_waitcnt vmcnt(8)
	s_waitcnt lgkmcnt(0)
	s_barrier
	s_setprio 1
	s_waitcnt lgkmcnt(0)
	v_mfma_f32_16x16x32_bf16 v[128:131], v[148:151], v[190:193], v[128:131]
	v_mfma_f32_16x16x32_bf16 v[124:127], v[156:159], v[190:193], v[124:127]
	v_mfma_f32_16x16x32_bf16 v[112:115], v[148:151], v[216:219], v[112:115]
	v_mfma_f32_16x16x32_bf16 v[108:111], v[156:159], v[216:219], v[108:111]
	v_mfma_f32_16x16x32_bf16 v[96:99], v[148:151], v[228:231], v[96:99]
	v_mfma_f32_16x16x32_bf16 v[92:95], v[156:159], v[228:231], v[92:95]
	v_mfma_f32_16x16x32_bf16 v[80:83], v[148:151], v[236:239], v[80:83]
	v_mfma_f32_16x16x32_bf16 v[76:79], v[156:159], v[236:239], v[76:79]
	v_mfma_f32_16x16x32_bf16 v[128:131], v[152:155], v[212:215], v[128:131]
	v_mfma_f32_16x16x32_bf16 v[124:127], v[160:163], v[212:215], v[124:127]
	v_mfma_f32_16x16x32_bf16 v[112:115], v[152:155], v[224:227], v[112:115]
	v_mfma_f32_16x16x32_bf16 v[108:111], v[160:163], v[224:227], v[108:111]
	v_mfma_f32_16x16x32_bf16 v[96:99], v[152:155], v[232:235], v[96:99]
	v_mfma_f32_16x16x32_bf16 v[92:95], v[160:163], v[232:235], v[92:95]
	v_mfma_f32_16x16x32_bf16 v[80:83], v[152:155], v[240:243], v[80:83]
	v_mfma_f32_16x16x32_bf16 v[76:79], v[160:163], v[240:243], v[76:79]
	v_mfma_f32_16x16x32_bf16 v[120:123], v[170:173], v[190:193], v[120:123]
	v_mfma_f32_16x16x32_bf16 v[116:119], v[178:181], v[190:193], v[116:119]
	v_mfma_f32_16x16x32_bf16 v[104:107], v[170:173], v[216:219], v[104:107]
	v_mfma_f32_16x16x32_bf16 v[100:103], v[178:181], v[216:219], v[100:103]
	v_mfma_f32_16x16x32_bf16 v[88:91], v[170:173], v[228:231], v[88:91]
	v_mfma_f32_16x16x32_bf16 v[84:87], v[178:181], v[228:231], v[84:87]
	v_mfma_f32_16x16x32_bf16 v[72:75], v[170:173], v[236:239], v[72:75]
	v_mfma_f32_16x16x32_bf16 v[68:71], v[178:181], v[236:239], v[68:71]
	v_mfma_f32_16x16x32_bf16 v[120:123], v[174:177], v[212:215], v[120:123]
	v_mfma_f32_16x16x32_bf16 v[116:119], v[182:185], v[212:215], v[116:119]
	v_mfma_f32_16x16x32_bf16 v[104:107], v[174:177], v[224:227], v[104:107]
	v_mfma_f32_16x16x32_bf16 v[100:103], v[182:185], v[224:227], v[100:103]
	v_mfma_f32_16x16x32_bf16 v[88:91], v[174:177], v[232:235], v[88:91]
	v_mfma_f32_16x16x32_bf16 v[84:87], v[182:185], v[232:235], v[84:87]
	v_mfma_f32_16x16x32_bf16 v[72:75], v[174:177], v[240:243], v[72:75]
	v_mfma_f32_16x16x32_bf16 v[68:71], v[182:185], v[240:243], v[68:71]
	s_setprio 0
	s_barrier
	s_add_i32 s2, s2, s17
	v_lshl_add_u64 v[164:165], s[34:35], 0, v[132:133]
	s_mov_b32 m0, s2
	ds_read_b128 v[190:193], v169 offset:16384
	ds_read_b128 v[212:215], v169 offset:17408
	ds_read_b128 v[216:219], v169 offset:18432
	ds_read_b128 v[224:227], v169 offset:19456
	ds_read_b128 v[228:231], v169 offset:20480
	ds_read_b128 v[232:235], v169 offset:21504
	ds_read_b128 v[236:239], v169 offset:22528
	ds_read_b128 v[240:243], v169 offset:23552
	global_load_lds_dwordx4 v[164:165], off
	s_add_i32 m0, s2, 0x2000
	s_add_u32 s2, s34, 0x20000
	v_lshl_add_u64 v[186:187], s[34:35], 0, v[134:135]
	s_addc_u32 s3, s35, 0
	s_add_i32 s58, s58, s17
	global_load_lds_dwordx4 v[186:187], off
	v_lshl_add_u64 v[194:195], s[2:3], 0, v[132:133]
	s_mov_b32 m0, s58
	v_lshl_add_u64 v[244:245], s[36:37], 0, v[138:139]
	global_load_lds_dwordx4 v[194:195], off
	v_lshl_add_u64 v[194:195], s[2:3], 0, v[134:135]
	s_add_i32 m0, s58, 0x2000
	s_nop 0
	global_load_lds_dwordx4 v[194:195], off
	v_lshl_add_u64 v[194:195], s[36:37], 0, v[136:137]
	s_mov_b32 m0, s18
	s_nop 0
	global_load_lds_dwordx4 v[194:195], off
	s_mov_b32 m0, s19
	s_nop 0
	global_load_lds_dwordx4 v[244:245], off
	s_waitcnt vmcnt(8)
	s_waitcnt lgkmcnt(0)
	s_barrier
	s_setprio 1
	s_waitcnt lgkmcnt(0)
	v_mfma_f32_16x16x32_bf16 v[64:67], v[148:151], v[190:193], v[64:67]
	v_mfma_f32_16x16x32_bf16 v[60:63], v[156:159], v[190:193], v[60:63]
	v_mfma_f32_16x16x32_bf16 v[48:51], v[148:151], v[216:219], v[48:51]
	v_mfma_f32_16x16x32_bf16 v[44:47], v[156:159], v[216:219], v[44:47]
	v_mfma_f32_16x16x32_bf16 v[32:35], v[148:151], v[228:231], v[32:35]
	v_mfma_f32_16x16x32_bf16 v[28:31], v[156:159], v[228:231], v[28:31]
	v_mfma_f32_16x16x32_bf16 v[16:19], v[148:151], v[236:239], v[16:19]
	v_mfma_f32_16x16x32_bf16 v[12:15], v[156:159], v[236:239], v[12:15]
	v_mfma_f32_16x16x32_bf16 v[64:67], v[152:155], v[212:215], v[64:67]
	v_mfma_f32_16x16x32_bf16 v[60:63], v[160:163], v[212:215], v[60:63]
	v_mfma_f32_16x16x32_bf16 v[48:51], v[152:155], v[224:227], v[48:51]
	v_mfma_f32_16x16x32_bf16 v[44:47], v[160:163], v[224:227], v[44:47]
	v_mfma_f32_16x16x32_bf16 v[32:35], v[152:155], v[232:235], v[32:35]
	v_mfma_f32_16x16x32_bf16 v[28:31], v[160:163], v[232:235], v[28:31]
	v_mfma_f32_16x16x32_bf16 v[16:19], v[152:155], v[240:243], v[16:19]
	v_mfma_f32_16x16x32_bf16 v[12:15], v[160:163], v[240:243], v[12:15]
	v_mfma_f32_16x16x32_bf16 v[52:55], v[170:173], v[190:193], v[52:55]
	v_mfma_f32_16x16x32_bf16 v[56:59], v[178:181], v[190:193], v[56:59]
	v_mfma_f32_16x16x32_bf16 v[36:39], v[170:173], v[216:219], v[36:39]
	v_mfma_f32_16x16x32_bf16 v[40:43], v[178:181], v[216:219], v[40:43]
	v_mfma_f32_16x16x32_bf16 v[20:23], v[170:173], v[228:231], v[20:23]
	v_mfma_f32_16x16x32_bf16 v[24:27], v[178:181], v[228:231], v[24:27]
	v_mfma_f32_16x16x32_bf16 v[4:7], v[170:173], v[236:239], v[4:7]
	v_mfma_f32_16x16x32_bf16 v[8:11], v[178:181], v[236:239], v[8:11]
	v_mfma_f32_16x16x32_bf16 v[52:55], v[174:177], v[212:215], v[52:55]
	v_mfma_f32_16x16x32_bf16 v[56:59], v[182:185], v[212:215], v[56:59]
	v_mfma_f32_16x16x32_bf16 v[36:39], v[174:177], v[224:227], v[36:39]
	v_mfma_f32_16x16x32_bf16 v[40:43], v[182:185], v[224:227], v[40:43]
	v_mfma_f32_16x16x32_bf16 v[20:23], v[174:177], v[232:235], v[20:23]
	v_mfma_f32_16x16x32_bf16 v[24:27], v[182:185], v[232:235], v[24:27]
	v_mfma_f32_16x16x32_bf16 v[4:7], v[174:177], v[240:243], v[4:7]
	v_mfma_f32_16x16x32_bf16 v[8:11], v[182:185], v[240:243], v[8:11]
	s_setprio 0
	s_barrier
	s_add_i32 s2, 0, 0x18000
	v_add_u32_e32 v2, s2, v168
	s_add_i32 s58, 0, 0x1c000
	ds_read_b128 v[148:151], v2
	ds_read_b128 v[152:155], v2 offset:1024
	ds_read_b128 v[156:159], v2 offset:2048
	ds_read_b128 v[160:163], v2 offset:3072
	v_add_u32_e32 v2, s58, v168
	ds_read_b128 v[170:173], v2
	ds_read_b128 v[174:177], v2 offset:1024
	ds_read_b128 v[178:181], v2 offset:2048
	ds_read_b128 v[182:185], v2 offset:3072
	s_mov_b32 m0, s20
	v_lshl_add_u64 v[246:247], s[36:37], 0, v[140:141]
	ds_read_b128 v[190:193], v169 offset:32768
	ds_read_b128 v[212:215], v169 offset:33792
	ds_read_b128 v[216:219], v169 offset:34816
	ds_read_b128 v[224:227], v169 offset:35840
	ds_read_b128 v[228:231], v169 offset:36864
	ds_read_b128 v[232:235], v169 offset:37888
	ds_read_b128 v[236:239], v169 offset:38912
	ds_read_b128 v[240:243], v169 offset:39936
	global_load_lds_dwordx4 v[246:247], off
	v_lshl_add_u64 v[246:247], s[36:37], 0, v[142:143]
	s_mov_b32 m0, s21
	s_nop 0
	global_load_lds_dwordx4 v[246:247], off
	s_waitcnt vmcnt(8)
	s_waitcnt lgkmcnt(0)
	s_barrier
	s_setprio 1
	s_waitcnt lgkmcnt(0)
	v_mfma_f32_16x16x32_bf16 v[128:131], v[148:151], v[190:193], v[128:131]
	v_mfma_f32_16x16x32_bf16 v[124:127], v[156:159], v[190:193], v[124:127]
	v_mfma_f32_16x16x32_bf16 v[112:115], v[148:151], v[216:219], v[112:115]
	v_mfma_f32_16x16x32_bf16 v[108:111], v[156:159], v[216:219], v[108:111]
	v_mfma_f32_16x16x32_bf16 v[96:99], v[148:151], v[228:231], v[96:99]
	v_mfma_f32_16x16x32_bf16 v[92:95], v[156:159], v[228:231], v[92:95]
	v_mfma_f32_16x16x32_bf16 v[80:83], v[148:151], v[236:239], v[80:83]
	v_mfma_f32_16x16x32_bf16 v[76:79], v[156:159], v[236:239], v[76:79]
	v_mfma_f32_16x16x32_bf16 v[128:131], v[152:155], v[212:215], v[128:131]
	v_mfma_f32_16x16x32_bf16 v[124:127], v[160:163], v[212:215], v[124:127]
	v_mfma_f32_16x16x32_bf16 v[112:115], v[152:155], v[224:227], v[112:115]
	v_mfma_f32_16x16x32_bf16 v[108:111], v[160:163], v[224:227], v[108:111]
	v_mfma_f32_16x16x32_bf16 v[96:99], v[152:155], v[232:235], v[96:99]
	v_mfma_f32_16x16x32_bf16 v[92:95], v[160:163], v[232:235], v[92:95]
	v_mfma_f32_16x16x32_bf16 v[80:83], v[152:155], v[240:243], v[80:83]
	v_mfma_f32_16x16x32_bf16 v[76:79], v[160:163], v[240:243], v[76:79]
	v_mfma_f32_16x16x32_bf16 v[120:123], v[170:173], v[190:193], v[120:123]
	v_mfma_f32_16x16x32_bf16 v[116:119], v[178:181], v[190:193], v[116:119]
	v_mfma_f32_16x16x32_bf16 v[104:107], v[170:173], v[216:219], v[104:107]
	v_mfma_f32_16x16x32_bf16 v[100:103], v[178:181], v[216:219], v[100:103]
	v_mfma_f32_16x16x32_bf16 v[88:91], v[170:173], v[228:231], v[88:91]
	v_mfma_f32_16x16x32_bf16 v[84:87], v[178:181], v[228:231], v[84:87]
	v_mfma_f32_16x16x32_bf16 v[72:75], v[170:173], v[236:239], v[72:75]
	v_mfma_f32_16x16x32_bf16 v[68:71], v[178:181], v[236:239], v[68:71]
	v_mfma_f32_16x16x32_bf16 v[120:123], v[174:177], v[212:215], v[120:123]
	v_mfma_f32_16x16x32_bf16 v[116:119], v[182:185], v[212:215], v[116:119]
	v_mfma_f32_16x16x32_bf16 v[104:107], v[174:177], v[224:227], v[104:107]
	v_mfma_f32_16x16x32_bf16 v[100:103], v[182:185], v[224:227], v[100:103]
	v_mfma_f32_16x16x32_bf16 v[88:91], v[174:177], v[232:235], v[88:91]
	v_mfma_f32_16x16x32_bf16 v[84:87], v[182:185], v[232:235], v[84:87]
	v_mfma_f32_16x16x32_bf16 v[72:75], v[174:177], v[240:243], v[72:75]
	v_mfma_f32_16x16x32_bf16 v[68:71], v[182:185], v[240:243], v[68:71]
	s_setprio 0
	s_barrier
	s_add_i32 s2, s2, s17
	v_lshl_add_u64 v[164:165], v[164:165], 0, s[30:31]
	s_mov_b32 m0, s2
	ds_read_b128 v[190:193], v169 offset:49152
	ds_read_b128 v[212:215], v169 offset:50176
	ds_read_b128 v[216:219], v169 offset:51200
	ds_read_b128 v[224:227], v169 offset:52224
	ds_read_b128 v[228:231], v169 offset:53248
	ds_read_b128 v[232:235], v169 offset:54272
	ds_read_b128 v[236:239], v169 offset:55296
	ds_read_b128 v[240:243], v169 offset:56320
	global_load_lds_dwordx4 v[164:165], off
	s_add_i32 m0, s2, 0x2000
	s_add_u32 s2, s34, 0x20080
	v_lshl_add_u64 v[164:165], v[186:187], 0, s[30:31]
	s_addc_u32 s3, s35, 0
	s_add_i32 s34, s58, s17
	global_load_lds_dwordx4 v[164:165], off
	v_lshl_add_u64 v[164:165], s[2:3], 0, v[132:133]
	s_mov_b32 m0, s34
	s_nop 0
	global_load_lds_dwordx4 v[164:165], off
	v_lshl_add_u64 v[164:165], s[2:3], 0, v[134:135]
	s_add_i32 m0, s34, 0x2000
	s_nop 0
	global_load_lds_dwordx4 v[164:165], off
	v_lshl_add_u64 v[164:165], v[194:195], 0, s[30:31]
	s_mov_b32 m0, s24
	s_nop 0
	global_load_lds_dwordx4 v[164:165], off
	v_lshl_add_u64 v[164:165], v[244:245], 0, s[30:31]
	s_mov_b32 m0, s25
	s_nop 0
	global_load_lds_dwordx4 v[164:165], off
	s_waitcnt vmcnt(8)
	s_waitcnt lgkmcnt(0)
	s_barrier
	s_setprio 1
	s_waitcnt lgkmcnt(0)
	v_mfma_f32_16x16x32_bf16 v[64:67], v[148:151], v[190:193], v[64:67]
	v_mfma_f32_16x16x32_bf16 v[60:63], v[156:159], v[190:193], v[60:63]
	v_mfma_f32_16x16x32_bf16 v[48:51], v[148:151], v[216:219], v[48:51]
	v_mfma_f32_16x16x32_bf16 v[44:47], v[156:159], v[216:219], v[44:47]
	v_mfma_f32_16x16x32_bf16 v[32:35], v[148:151], v[228:231], v[32:35]
	v_mfma_f32_16x16x32_bf16 v[28:31], v[156:159], v[228:231], v[28:31]
	v_mfma_f32_16x16x32_bf16 v[16:19], v[148:151], v[236:239], v[16:19]
	v_mfma_f32_16x16x32_bf16 v[12:15], v[156:159], v[236:239], v[12:15]
	v_mfma_f32_16x16x32_bf16 v[64:67], v[152:155], v[212:215], v[64:67]
	v_mfma_f32_16x16x32_bf16 v[60:63], v[160:163], v[212:215], v[60:63]
	v_mfma_f32_16x16x32_bf16 v[48:51], v[152:155], v[224:227], v[48:51]
	v_mfma_f32_16x16x32_bf16 v[44:47], v[160:163], v[224:227], v[44:47]
	v_mfma_f32_16x16x32_bf16 v[32:35], v[152:155], v[232:235], v[32:35]
	v_mfma_f32_16x16x32_bf16 v[28:31], v[160:163], v[232:235], v[28:31]
	v_mfma_f32_16x16x32_bf16 v[16:19], v[152:155], v[240:243], v[16:19]
	v_mfma_f32_16x16x32_bf16 v[12:15], v[160:163], v[240:243], v[12:15]
	v_mfma_f32_16x16x32_bf16 v[52:55], v[170:173], v[190:193], v[52:55]
	v_mfma_f32_16x16x32_bf16 v[56:59], v[178:181], v[190:193], v[56:59]
	v_mfma_f32_16x16x32_bf16 v[36:39], v[170:173], v[216:219], v[36:39]
	v_mfma_f32_16x16x32_bf16 v[40:43], v[178:181], v[216:219], v[40:43]
	v_mfma_f32_16x16x32_bf16 v[20:23], v[170:173], v[228:231], v[20:23]
	v_mfma_f32_16x16x32_bf16 v[24:27], v[178:181], v[228:231], v[24:27]
	v_mfma_f32_16x16x32_bf16 v[4:7], v[170:173], v[236:239], v[4:7]
	v_mfma_f32_16x16x32_bf16 v[8:11], v[178:181], v[236:239], v[8:11]
	v_mfma_f32_16x16x32_bf16 v[52:55], v[174:177], v[212:215], v[52:55]
	v_mfma_f32_16x16x32_bf16 v[56:59], v[182:185], v[212:215], v[56:59]
	v_mfma_f32_16x16x32_bf16 v[36:39], v[174:177], v[224:227], v[36:39]
	v_mfma_f32_16x16x32_bf16 v[40:43], v[182:185], v[224:227], v[40:43]
	v_mfma_f32_16x16x32_bf16 v[20:23], v[174:177], v[232:235], v[20:23]
	v_mfma_f32_16x16x32_bf16 v[24:27], v[182:185], v[232:235], v[24:27]
	v_mfma_f32_16x16x32_bf16 v[4:7], v[174:177], v[240:243], v[4:7]
	v_mfma_f32_16x16x32_bf16 v[8:11], v[182:185], v[240:243], v[8:11]
	s_setprio 0
	s_barrier
	s_add_i32 s57, s57, 2
	s_add_u32 s0, s0, 0x100
	s_addc_u32 s1, s1, 0
	s_add_u32 s29, s29, 0x100
	s_addc_u32 s56, s56, 0
	s_cmp_gt_u32 s57, 5
	s_cbranch_scc0 .LBB0_991
	s_and_b64 vcc, exec, s[42:43]
	s_cbranch_vccz .LBB0_994
	s_barrier

.LBB0_1105:
	s_add_u32 s62, s34, s7
	s_addc_u32 s63, s35, 0
	s_add_u32 s56, s62, 0x100
	s_addc_u32 s57, s63, 0
	s_and_b64 s[2:3], s[54:55], exec
	s_cselect_b32 s56, s44, s56
	s_cselect_b32 s57, s45, s57
	s_add_u32 s2, s50, s7
	s_addc_u32 s3, s51, 0
	s_add_u32 s7, s2, 0x100
	s_addc_u32 s58, s3, 0
	s_and_b64 s[2:3], s[54:55], exec
	s_cselect_b32 s59, s49, s58
	s_cselect_b32 s58, s48, s7
	s_add_i32 s55, 0, 0x10000
	s_add_i32 s69, 0, 0x14000
	v_add_u32_e32 v2, s55, v152
	s_add_i32 s68, s55, s17
	ds_read_b128 v[132:135], v2
	ds_read_b128 v[154:157], v2 offset:1024
	ds_read_b128 v[158:161], v2 offset:2048
	ds_read_b128 v[162:165], v2 offset:3072
	v_add_u32_e32 v2, s69, v152
	s_add_i32 m0, s18, 0xc000
	s_add_i32 s71, s18, 0xe000
	s_add_i32 s65, s68, 0x2000
	ds_read_b128 v[166:169], v2
	ds_read_b128 v[170:173], v2 offset:1024
	ds_read_b128 v[174:177], v2 offset:2048
	ds_read_b128 v[178:181], v2 offset:3072
	s_add_u32 s60, s58, 0x10000
	s_addc_u32 s61, s59, 0
	s_add_i32 s3, 0, 0x18000
	s_add_i32 s67, s69, s17
	s_add_i32 s64, s3, s17
	s_add_i32 s66, s67, 0x2000
	s_add_i32 s2, 0, 0x1c000
	s_add_i32 s7, s64, 0x2000
	s_add_u32 s54, s58, 0x10080
	s_addc_u32 s55, s59, 0
	s_add_i32 s70, s2, s17
	s_add_i32 s69, s70, 0x2000
	v_lshl_add_u64 v[148:149], s[62:63], 0, v[144:145]
	v_lshl_add_u64 v[148:149], v[148:149], 0, s[30:31]
	ds_read_b128 v[182:185], v153
	ds_read_b128 v[190:193], v153 offset:1024
	ds_read_b128 v[212:215], v153 offset:2048
	ds_read_b128 v[216:219], v153 offset:3072
	ds_read_b128 v[224:227], v153 offset:4096
	ds_read_b128 v[228:231], v153 offset:5120
	ds_read_b128 v[232:235], v153 offset:6144
	ds_read_b128 v[236:239], v153 offset:7168
	global_load_lds_dwordx4 v[148:149], off
	v_lshl_add_u64 v[148:149], s[62:63], 0, v[146:147]
	v_lshl_add_u64 v[148:149], v[148:149], 0, s[30:31]
	s_mov_b32 m0, s71
	s_nop 0
	global_load_lds_dwordx4 v[148:149], off
	s_waitcnt vmcnt(8)
	s_waitcnt lgkmcnt(0)
	s_barrier
	s_setprio 1
	s_waitcnt lgkmcnt(0)
	v_mfma_f32_16x16x32_bf16 v[128:131], v[132:135], v[182:185], v[128:131]
	v_mfma_f32_16x16x32_bf16 v[124:127], v[158:161], v[182:185], v[124:127]
	v_mfma_f32_16x16x32_bf16 v[112:115], v[132:135], v[212:215], v[112:115]
	v_mfma_f32_16x16x32_bf16 v[108:111], v[158:161], v[212:215], v[108:111]
	v_mfma_f32_16x16x32_bf16 v[96:99], v[132:135], v[224:227], v[96:99]
	v_mfma_f32_16x16x32_bf16 v[92:95], v[158:161], v[224:227], v[92:95]
	v_mfma_f32_16x16x32_bf16 v[80:83], v[132:135], v[232:235], v[80:83]
	v_mfma_f32_16x16x32_bf16 v[76:79], v[158:161], v[232:235], v[76:79]
	v_mfma_f32_16x16x32_bf16 v[128:131], v[154:157], v[190:193], v[128:131]
	v_mfma_f32_16x16x32_bf16 v[124:127], v[162:165], v[190:193], v[124:127]
	v_mfma_f32_16x16x32_bf16 v[112:115], v[154:157], v[216:219], v[112:115]
	v_mfma_f32_16x16x32_bf16 v[108:111], v[162:165], v[216:219], v[108:111]
	v_mfma_f32_16x16x32_bf16 v[96:99], v[154:157], v[228:231], v[96:99]
	v_mfma_f32_16x16x32_bf16 v[92:95], v[162:165], v[228:231], v[92:95]
	v_mfma_f32_16x16x32_bf16 v[80:83], v[154:157], v[236:239], v[80:83]
	v_mfma_f32_16x16x32_bf16 v[76:79], v[162:165], v[236:239], v[76:79]
	v_mfma_f32_16x16x32_bf16 v[120:123], v[166:169], v[182:185], v[120:123]
	v_mfma_f32_16x16x32_bf16 v[116:119], v[174:177], v[182:185], v[116:119]
	v_mfma_f32_16x16x32_bf16 v[104:107], v[166:169], v[212:215], v[104:107]
	v_mfma_f32_16x16x32_bf16 v[100:103], v[174:177], v[212:215], v[100:103]
	v_mfma_f32_16x16x32_bf16 v[88:91], v[166:169], v[224:227], v[88:91]
	v_mfma_f32_16x16x32_bf16 v[84:87], v[174:177], v[224:227], v[84:87]
	v_mfma_f32_16x16x32_bf16 v[72:75], v[166:169], v[232:235], v[72:75]
	v_mfma_f32_16x16x32_bf16 v[68:71], v[174:177], v[232:235], v[68:71]
	v_mfma_f32_16x16x32_bf16 v[120:123], v[170:173], v[190:193], v[120:123]
	v_mfma_f32_16x16x32_bf16 v[116:119], v[178:181], v[190:193], v[116:119]
	v_mfma_f32_16x16x32_bf16 v[104:107], v[170:173], v[216:219], v[104:107]
	v_mfma_f32_16x16x32_bf16 v[100:103], v[178:181], v[216:219], v[100:103]
	v_mfma_f32_16x16x32_bf16 v[88:91], v[170:173], v[228:231], v[88:91]
	v_mfma_f32_16x16x32_bf16 v[84:87], v[178:181], v[228:231], v[84:87]
	v_mfma_f32_16x16x32_bf16 v[72:75], v[170:173], v[236:239], v[72:75]
	v_mfma_f32_16x16x32_bf16 v[68:71], v[178:181], v[236:239], v[68:71]
	s_setprio 0
	s_barrier
	s_mov_b32 m0, s68
	v_lshl_add_u64 v[148:149], s[58:59], 0, v[136:137]
	ds_read_b128 v[182:185], v153 offset:16384
	ds_read_b128 v[190:193], v153 offset:17408
	ds_read_b128 v[212:215], v153 offset:18432
	ds_read_b128 v[216:219], v153 offset:19456
	ds_read_b128 v[224:227], v153 offset:20480
	ds_read_b128 v[228:231], v153 offset:21504
	ds_read_b128 v[232:235], v153 offset:22528
	ds_read_b128 v[236:239], v153 offset:23552
	global_load_lds_dwordx4 v[148:149], off
	v_lshl_add_u64 v[186:187], s[58:59], 0, v[138:139]
	s_mov_b32 m0, s65
	v_lshl_add_u64 v[194:195], s[60:61], 0, v[136:137]
	global_load_lds_dwordx4 v[186:187], off
	s_mov_b32 m0, s67
	v_lshl_add_u64 v[240:241], s[56:57], 0, v[142:143]
	global_load_lds_dwordx4 v[194:195], off
	v_lshl_add_u64 v[194:195], s[60:61], 0, v[138:139]
	s_mov_b32 m0, s66
	s_nop 0
	global_load_lds_dwordx4 v[194:195], off
	v_lshl_add_u64 v[194:195], s[56:57], 0, v[140:141]
	s_mov_b32 m0, s18
	s_nop 0
	global_load_lds_dwordx4 v[194:195], off
	s_mov_b32 m0, s19
	s_nop 0
	global_load_lds_dwordx4 v[240:241], off
	s_waitcnt vmcnt(8)
	s_waitcnt lgkmcnt(0)
	s_barrier
	s_setprio 1
	s_waitcnt lgkmcnt(0)
	v_mfma_f32_16x16x32_bf16 v[56:59], v[132:135], v[182:185], v[56:59]
	v_mfma_f32_16x16x32_bf16 v[52:55], v[158:161], v[182:185], v[52:55]
	v_mfma_f32_16x16x32_bf16 v[40:43], v[132:135], v[212:215], v[40:43]
	v_mfma_f32_16x16x32_bf16 v[36:39], v[158:161], v[212:215], v[36:39]
	v_mfma_f32_16x16x32_bf16 v[24:27], v[132:135], v[224:227], v[24:27]
	v_mfma_f32_16x16x32_bf16 v[20:23], v[158:161], v[224:227], v[20:23]
	v_mfma_f32_16x16x32_bf16 v[8:11], v[132:135], v[232:235], v[8:11]
	v_mfma_f32_16x16x32_bf16 v[4:7], v[158:161], v[232:235], v[4:7]
	v_mfma_f32_16x16x32_bf16 v[56:59], v[154:157], v[190:193], v[56:59]
	v_mfma_f32_16x16x32_bf16 v[52:55], v[162:165], v[190:193], v[52:55]
	v_mfma_f32_16x16x32_bf16 v[40:43], v[154:157], v[216:219], v[40:43]
	v_mfma_f32_16x16x32_bf16 v[36:39], v[162:165], v[216:219], v[36:39]
	v_mfma_f32_16x16x32_bf16 v[24:27], v[154:157], v[228:231], v[24:27]
	v_mfma_f32_16x16x32_bf16 v[20:23], v[162:165], v[228:231], v[20:23]
	v_mfma_f32_16x16x32_bf16 v[8:11], v[154:157], v[236:239], v[8:11]
	v_mfma_f32_16x16x32_bf16 v[4:7], v[162:165], v[236:239], v[4:7]
	v_mfma_f32_16x16x32_bf16 v[60:63], v[166:169], v[182:185], v[60:63]
	v_mfma_f32_16x16x32_bf16 v[64:67], v[174:177], v[182:185], v[64:67]
	v_mfma_f32_16x16x32_bf16 v[44:47], v[166:169], v[212:215], v[44:47]
	v_mfma_f32_16x16x32_bf16 v[48:51], v[174:177], v[212:215], v[48:51]
	v_mfma_f32_16x16x32_bf16 v[28:31], v[166:169], v[224:227], v[28:31]
	v_mfma_f32_16x16x32_bf16 v[32:35], v[174:177], v[224:227], v[32:35]
	v_mfma_f32_16x16x32_bf16 v[12:15], v[166:169], v[232:235], v[12:15]
	v_mfma_f32_16x16x32_bf16 v[16:19], v[174:177], v[232:235], v[16:19]
	v_mfma_f32_16x16x32_bf16 v[60:63], v[170:173], v[190:193], v[60:63]
	v_mfma_f32_16x16x32_bf16 v[64:67], v[178:181], v[190:193], v[64:67]
	v_mfma_f32_16x16x32_bf16 v[44:47], v[170:173], v[216:219], v[44:47]
	v_mfma_f32_16x16x32_bf16 v[48:51], v[178:181], v[216:219], v[48:51]
	v_mfma_f32_16x16x32_bf16 v[28:31], v[170:173], v[228:231], v[28:31]
	v_mfma_f32_16x16x32_bf16 v[32:35], v[178:181], v[228:231], v[32:35]
	v_mfma_f32_16x16x32_bf16 v[12:15], v[170:173], v[236:239], v[12:15]
	v_mfma_f32_16x16x32_bf16 v[16:19], v[178:181], v[236:239], v[16:19]
	s_setprio 0
	s_barrier
	v_add_u32_e32 v2, s3, v152
	ds_read_b128 v[132:135], v2
	ds_read_b128 v[154:157], v2 offset:1024
	ds_read_b128 v[158:161], v2 offset:2048
	ds_read_b128 v[162:165], v2 offset:3072
	v_add_u32_e32 v2, s2, v152
	ds_read_b128 v[166:169], v2
	ds_read_b128 v[170:173], v2 offset:1024
	ds_read_b128 v[174:177], v2 offset:2048
	ds_read_b128 v[178:181], v2 offset:3072
	s_mov_b32 m0, s20
	v_lshl_add_u64 v[242:243], s[56:57], 0, v[144:145]
	ds_read_b128 v[182:185], v153 offset:32768
	ds_read_b128 v[190:193], v153 offset:33792
	ds_read_b128 v[212:215], v153 offset:34816
	ds_read_b128 v[216:219], v153 offset:35840
	ds_read_b128 v[224:227], v153 offset:36864
	ds_read_b128 v[228:231], v153 offset:37888
	ds_read_b128 v[232:235], v153 offset:38912
	ds_read_b128 v[236:239], v153 offset:39936
	global_load_lds_dwordx4 v[242:243], off
	v_lshl_add_u64 v[242:243], s[56:57], 0, v[146:147]
	s_mov_b32 m0, s21
	s_nop 0
	global_load_lds_dwordx4 v[242:243], off
	s_waitcnt vmcnt(8)
	s_waitcnt lgkmcnt(0)
	s_barrier
	s_setprio 1
	s_waitcnt lgkmcnt(0)
	v_mfma_f32_16x16x32_bf16 v[128:131], v[132:135], v[182:185], v[128:131]
	v_mfma_f32_16x16x32_bf16 v[124:127], v[158:161], v[182:185], v[124:127]
	v_mfma_f32_16x16x32_bf16 v[112:115], v[132:135], v[212:215], v[112:115]
	v_mfma_f32_16x16x32_bf16 v[108:111], v[158:161], v[212:215], v[108:111]
	v_mfma_f32_16x16x32_bf16 v[96:99], v[132:135], v[224:227], v[96:99]
	v_mfma_f32_16x16x32_bf16 v[92:95], v[158:161], v[224:227], v[92:95]
	v_mfma_f32_16x16x32_bf16 v[80:83], v[132:135], v[232:235], v[80:83]
	v_mfma_f32_16x16x32_bf16 v[76:79], v[158:161], v[232:235], v[76:79]
	v_mfma_f32_16x16x32_bf16 v[128:131], v[154:157], v[190:193], v[128:131]
	v_mfma_f32_16x16x32_bf16 v[124:127], v[162:165], v[190:193], v[124:127]
	v_mfma_f32_16x16x32_bf16 v[112:115], v[154:157], v[216:219], v[112:115]
	v_mfma_f32_16x16x32_bf16 v[108:111], v[162:165], v[216:219], v[108:111]
	v_mfma_f32_16x16x32_bf16 v[96:99], v[154:157], v[228:231], v[96:99]
	v_mfma_f32_16x16x32_bf16 v[92:95], v[162:165], v[228:231], v[92:95]
	v_mfma_f32_16x16x32_bf16 v[80:83], v[154:157], v[236:239], v[80:83]
	v_mfma_f32_16x16x32_bf16 v[76:79], v[162:165], v[236:239], v[76:79]
	v_mfma_f32_16x16x32_bf16 v[120:123], v[166:169], v[182:185], v[120:123]
	v_mfma_f32_16x16x32_bf16 v[116:119], v[174:177], v[182:185], v[116:119]
	v_mfma_f32_16x16x32_bf16 v[104:107], v[166:169], v[212:215], v[104:107]
	v_mfma_f32_16x16x32_bf16 v[100:103], v[174:177], v[212:215], v[100:103]
	v_mfma_f32_16x16x32_bf16 v[88:91], v[166:169], v[224:227], v[88:91]
	v_mfma_f32_16x16x32_bf16 v[84:87], v[174:177], v[224:227], v[84:87]
	v_mfma_f32_16x16x32_bf16 v[72:75], v[166:169], v[232:235], v[72:75]
	v_mfma_f32_16x16x32_bf16 v[68:71], v[174:177], v[232:235], v[68:71]
	v_mfma_f32_16x16x32_bf16 v[120:123], v[170:173], v[190:193], v[120:123]
	v_mfma_f32_16x16x32_bf16 v[116:119], v[178:181], v[190:193], v[116:119]
	v_mfma_f32_16x16x32_bf16 v[104:107], v[170:173], v[216:219], v[104:107]
	v_mfma_f32_16x16x32_bf16 v[100:103], v[178:181], v[216:219], v[100:103]
	v_mfma_f32_16x16x32_bf16 v[88:91], v[170:173], v[228:231], v[88:91]
	v_mfma_f32_16x16x32_bf16 v[84:87], v[178:181], v[228:231], v[84:87]
	v_mfma_f32_16x16x32_bf16 v[72:75], v[170:173], v[236:239], v[72:75]
	v_mfma_f32_16x16x32_bf16 v[68:71], v[178:181], v[236:239], v[68:71]
	s_setprio 0
	s_barrier
	s_mov_b32 m0, s64
	v_lshl_add_u64 v[148:149], v[148:149], 0, s[30:31]
	ds_read_b128 v[182:185], v153 offset:49152
	ds_read_b128 v[190:193], v153 offset:50176
	ds_read_b128 v[212:215], v153 offset:51200
	ds_read_b128 v[216:219], v153 offset:52224
	ds_read_b128 v[224:227], v153 offset:53248
	ds_read_b128 v[228:231], v153 offset:54272
	ds_read_b128 v[232:235], v153 offset:55296
	ds_read_b128 v[236:239], v153 offset:56320
	global_load_lds_dwordx4 v[148:149], off
	v_lshl_add_u64 v[148:149], v[186:187], 0, s[30:31]
	s_mov_b32 m0, s7
	s_nop 0
	global_load_lds_dwordx4 v[148:149], off
	v_lshl_add_u64 v[148:149], s[54:55], 0, v[136:137]
	s_mov_b32 m0, s70
	s_nop 0
	global_load_lds_dwordx4 v[148:149], off
	v_lshl_add_u64 v[148:149], s[54:55], 0, v[138:139]
	s_mov_b32 m0, s69
	s_nop 0
	global_load_lds_dwordx4 v[148:149], off
	v_lshl_add_u64 v[148:149], v[194:195], 0, s[30:31]
	s_mov_b32 m0, s24
	s_nop 0
	global_load_lds_dwordx4 v[148:149], off
	v_lshl_add_u64 v[148:149], v[240:241], 0, s[30:31]
	s_mov_b32 m0, s25
	s_nop 0
	global_load_lds_dwordx4 v[148:149], off
	s_waitcnt vmcnt(8)
	s_waitcnt lgkmcnt(0)
	s_barrier
	s_setprio 1
	s_waitcnt lgkmcnt(0)
	v_mfma_f32_16x16x32_bf16 v[56:59], v[132:135], v[182:185], v[56:59]
	v_mfma_f32_16x16x32_bf16 v[52:55], v[158:161], v[182:185], v[52:55]
	v_mfma_f32_16x16x32_bf16 v[40:43], v[132:135], v[212:215], v[40:43]
	v_mfma_f32_16x16x32_bf16 v[36:39], v[158:161], v[212:215], v[36:39]
	v_mfma_f32_16x16x32_bf16 v[24:27], v[132:135], v[224:227], v[24:27]
	v_mfma_f32_16x16x32_bf16 v[20:23], v[158:161], v[224:227], v[20:23]
	v_mfma_f32_16x16x32_bf16 v[8:11], v[132:135], v[232:235], v[8:11]
	v_mfma_f32_16x16x32_bf16 v[4:7], v[158:161], v[232:235], v[4:7]
	v_mfma_f32_16x16x32_bf16 v[56:59], v[154:157], v[190:193], v[56:59]
	v_mfma_f32_16x16x32_bf16 v[52:55], v[162:165], v[190:193], v[52:55]
	v_mfma_f32_16x16x32_bf16 v[40:43], v[154:157], v[216:219], v[40:43]
	v_mfma_f32_16x16x32_bf16 v[36:39], v[162:165], v[216:219], v[36:39]
	v_mfma_f32_16x16x32_bf16 v[24:27], v[154:157], v[228:231], v[24:27]
	v_mfma_f32_16x16x32_bf16 v[20:23], v[162:165], v[228:231], v[20:23]
	v_mfma_f32_16x16x32_bf16 v[8:11], v[154:157], v[236:239], v[8:11]
	v_mfma_f32_16x16x32_bf16 v[4:7], v[162:165], v[236:239], v[4:7]
	v_mfma_f32_16x16x32_bf16 v[60:63], v[166:169], v[182:185], v[60:63]
	v_mfma_f32_16x16x32_bf16 v[64:67], v[174:177], v[182:185], v[64:67]
	v_mfma_f32_16x16x32_bf16 v[44:47], v[166:169], v[212:215], v[44:47]
	v_mfma_f32_16x16x32_bf16 v[48:51], v[174:177], v[212:215], v[48:51]
	v_mfma_f32_16x16x32_bf16 v[28:31], v[166:169], v[224:227], v[28:31]
	v_mfma_f32_16x16x32_bf16 v[32:35], v[174:177], v[224:227], v[32:35]
	v_mfma_f32_16x16x32_bf16 v[12:15], v[166:169], v[232:235], v[12:15]
	v_mfma_f32_16x16x32_bf16 v[16:19], v[174:177], v[232:235], v[16:19]
	v_mfma_f32_16x16x32_bf16 v[60:63], v[170:173], v[190:193], v[60:63]
	v_mfma_f32_16x16x32_bf16 v[64:67], v[178:181], v[190:193], v[64:67]
	v_mfma_f32_16x16x32_bf16 v[44:47], v[170:173], v[216:219], v[44:47]
	v_mfma_f32_16x16x32_bf16 v[48:51], v[178:181], v[216:219], v[48:51]
	v_mfma_f32_16x16x32_bf16 v[28:31], v[170:173], v[228:231], v[28:31]
	v_mfma_f32_16x16x32_bf16 v[32:35], v[178:181], v[228:231], v[32:35]
	v_mfma_f32_16x16x32_bf16 v[12:15], v[170:173], v[236:239], v[12:15]
	v_mfma_f32_16x16x32_bf16 v[16:19], v[178:181], v[236:239], v[16:19]
	s_setprio 0
	s_barrier
	s_movk_i32 s7, 0x100
	s_andn2_b64 vcc, exec, s[52:53]
	s_mov_b64 s[54:55], -1
	s_mov_b64 s[52:53], 0
	s_cbranch_vccz .LBB0_1105
	s_and_b64 vcc, exec, s[36:37]
	s_cbranch_vccz .LBB0_1108
	s_barrier

.LBB0_1295:
	s_add_u32 s2, s46, 0x80
	s_addc_u32 s3, s47, 0
	s_cmp_eq_u32 s53, 4
	s_cselect_b32 s51, s25, s3
	s_cselect_b32 s50, s26, s2
	s_cselect_b32 s49, s27, s52
	s_cselect_b32 s48, s28, s29
	s_add_i32 s2, 0, 0x10000
	v_add_u32_e32 v155, s2, v148
	s_add_i32 s54, 0, 0x14000
	ds_read_b128 v[150:153], v155
	ds_read_b128 v[156:159], v155 offset:1024
	ds_read_b128 v[160:163], v155 offset:2048
	ds_read_b128 v[164:167], v155 offset:3072
	v_add_u32_e32 v155, s54, v148
	ds_read_b128 v[168:171], v155
	ds_read_b128 v[172:175], v155 offset:1024
	ds_read_b128 v[176:179], v155 offset:2048
	ds_read_b128 v[180:183], v155 offset:3072
	v_lshl_add_u64 v[194:195], s[46:47], 0, v[144:145]
	s_add_i32 m0, s15, 0xc000
	ds_read_b128 v[184:187], v149
	ds_read_b128 v[190:193], v149 offset:1024
	ds_read_b128 v[212:215], v149 offset:2048
	ds_read_b128 v[216:219], v149 offset:3072
	ds_read_b128 v[224:227], v149 offset:4096
	ds_read_b128 v[228:231], v149 offset:5120
	ds_read_b128 v[232:235], v149 offset:6144
	ds_read_b128 v[236:239], v149 offset:7168
	global_load_lds_dwordx4 v[194:195], off
	v_lshl_add_u64 v[194:195], s[46:47], 0, v[142:143]
	s_add_i32 m0, s15, 0xe000
	s_nop 0
	global_load_lds_dwordx4 v[194:195], off
	s_waitcnt vmcnt(8)
	s_waitcnt lgkmcnt(0)
	s_barrier
	s_setprio 1
	s_waitcnt lgkmcnt(0)
	v_mfma_f32_16x16x32_bf16 v[128:131], v[150:153], v[184:187], v[128:131]
	v_mfma_f32_16x16x32_bf16 v[124:127], v[160:163], v[184:187], v[124:127]
	v_mfma_f32_16x16x32_bf16 v[120:123], v[150:153], v[212:215], v[120:123]
	v_mfma_f32_16x16x32_bf16 v[116:119], v[160:163], v[212:215], v[116:119]
	v_mfma_f32_16x16x32_bf16 v[104:107], v[150:153], v[224:227], v[104:107]
	v_mfma_f32_16x16x32_bf16 v[100:103], v[160:163], v[224:227], v[100:103]
	v_mfma_f32_16x16x32_bf16 v[88:91], v[150:153], v[232:235], v[88:91]
	v_mfma_f32_16x16x32_bf16 v[84:87], v[160:163], v[232:235], v[84:87]
	v_mfma_f32_16x16x32_bf16 v[128:131], v[156:159], v[190:193], v[128:131]
	v_mfma_f32_16x16x32_bf16 v[124:127], v[164:167], v[190:193], v[124:127]
	v_mfma_f32_16x16x32_bf16 v[120:123], v[156:159], v[216:219], v[120:123]
	v_mfma_f32_16x16x32_bf16 v[116:119], v[164:167], v[216:219], v[116:119]
	v_mfma_f32_16x16x32_bf16 v[104:107], v[156:159], v[228:231], v[104:107]
	v_mfma_f32_16x16x32_bf16 v[100:103], v[164:167], v[228:231], v[100:103]
	v_mfma_f32_16x16x32_bf16 v[88:91], v[156:159], v[236:239], v[88:91]
	v_mfma_f32_16x16x32_bf16 v[84:87], v[164:167], v[236:239], v[84:87]
	v_mfma_f32_16x16x32_bf16 v[112:115], v[168:171], v[184:187], v[112:115]
	v_mfma_f32_16x16x32_bf16 v[108:111], v[176:179], v[184:187], v[108:111]
	v_mfma_f32_16x16x32_bf16 v[96:99], v[168:171], v[212:215], v[96:99]
	v_mfma_f32_16x16x32_bf16 v[92:95], v[176:179], v[212:215], v[92:95]
	v_mfma_f32_16x16x32_bf16 v[76:79], v[168:171], v[224:227], v[76:79]
	v_mfma_f32_16x16x32_bf16 v[68:71], v[176:179], v[224:227], v[68:71]
	v_mfma_f32_16x16x32_bf16 v[56:59], v[168:171], v[232:235], v[56:59]
	v_mfma_f32_16x16x32_bf16 v[44:47], v[176:179], v[232:235], v[44:47]
	v_mfma_f32_16x16x32_bf16 v[112:115], v[172:175], v[190:193], v[112:115]
	v_mfma_f32_16x16x32_bf16 v[108:111], v[180:183], v[190:193], v[108:111]
	v_mfma_f32_16x16x32_bf16 v[96:99], v[172:175], v[216:219], v[96:99]
	v_mfma_f32_16x16x32_bf16 v[92:95], v[180:183], v[216:219], v[92:95]
	v_mfma_f32_16x16x32_bf16 v[76:79], v[172:175], v[228:231], v[76:79]
	v_mfma_f32_16x16x32_bf16 v[68:71], v[180:183], v[228:231], v[68:71]
	v_mfma_f32_16x16x32_bf16 v[56:59], v[172:175], v[236:239], v[56:59]
	v_mfma_f32_16x16x32_bf16 v[44:47], v[180:183], v[236:239], v[44:47]
	s_setprio 0
	s_barrier
	s_add_i32 s2, s2, s12
	v_lshl_add_u64 v[194:195], s[48:49], 0, v[2:3]
	s_mov_b32 m0, s2
	ds_read_b128 v[184:187], v149 offset:16384
	ds_read_b128 v[190:193], v149 offset:17408
	ds_read_b128 v[212:215], v149 offset:18432
	ds_read_b128 v[216:219], v149 offset:19456
	ds_read_b128 v[224:227], v149 offset:20480
	ds_read_b128 v[228:231], v149 offset:21504
	ds_read_b128 v[232:235], v149 offset:22528
	ds_read_b128 v[236:239], v149 offset:23552
	global_load_lds_dwordx4 v[194:195], off
	s_add_i32 m0, s2, 0x2000
	s_add_u32 s2, s48, 0x20000
	v_lshl_add_u64 v[240:241], s[48:49], 0, v[132:133]
	s_addc_u32 s3, s49, 0
	s_add_i32 s54, s54, s12
	global_load_lds_dwordx4 v[240:241], off
	v_lshl_add_u64 v[242:243], s[2:3], 0, v[2:3]
	s_mov_b32 m0, s54
	v_lshl_add_u64 v[244:245], s[50:51], 0, v[136:137]
	global_load_lds_dwordx4 v[242:243], off
	v_lshl_add_u64 v[242:243], s[2:3], 0, v[132:133]
	s_add_i32 m0, s54, 0x2000
	s_nop 0
	global_load_lds_dwordx4 v[242:243], off
	v_lshl_add_u64 v[242:243], s[50:51], 0, v[134:135]
	s_mov_b32 m0, s15
	s_nop 0
	global_load_lds_dwordx4 v[242:243], off
	s_mov_b32 m0, s16
	s_nop 0
	global_load_lds_dwordx4 v[244:245], off
	s_waitcnt vmcnt(8)
	s_waitcnt lgkmcnt(0)
	s_barrier
	s_setprio 1
	s_waitcnt lgkmcnt(0)
	v_mfma_f32_16x16x32_bf16 v[36:39], v[150:153], v[184:187], v[36:39]
	v_mfma_f32_16x16x32_bf16 v[28:31], v[160:163], v[184:187], v[28:31]
	v_mfma_f32_16x16x32_bf16 v[24:27], v[150:153], v[212:215], v[24:27]
	v_mfma_f32_16x16x32_bf16 v[20:23], v[160:163], v[212:215], v[20:23]
	v_mfma_f32_16x16x32_bf16 v[16:19], v[150:153], v[224:227], v[16:19]
	v_mfma_f32_16x16x32_bf16 v[12:15], v[160:163], v[224:227], v[12:15]
	v_mfma_f32_16x16x32_bf16 v[8:11], v[150:153], v[232:235], v[8:11]
	v_mfma_f32_16x16x32_bf16 v[4:7], v[160:163], v[232:235], v[4:7]
	v_mfma_f32_16x16x32_bf16 v[36:39], v[156:159], v[190:193], v[36:39]
	v_mfma_f32_16x16x32_bf16 v[28:31], v[164:167], v[190:193], v[28:31]
	v_mfma_f32_16x16x32_bf16 v[24:27], v[156:159], v[216:219], v[24:27]
	v_mfma_f32_16x16x32_bf16 v[20:23], v[164:167], v[216:219], v[20:23]
	v_mfma_f32_16x16x32_bf16 v[16:19], v[156:159], v[228:231], v[16:19]
	v_mfma_f32_16x16x32_bf16 v[12:15], v[164:167], v[228:231], v[12:15]
	v_mfma_f32_16x16x32_bf16 v[8:11], v[156:159], v[236:239], v[8:11]
	v_mfma_f32_16x16x32_bf16 v[4:7], v[164:167], v[236:239], v[4:7]
	v_mfma_f32_16x16x32_bf16 v[72:75], v[168:171], v[184:187], v[72:75]
	v_mfma_f32_16x16x32_bf16 v[80:83], v[176:179], v[184:187], v[80:83]
	v_mfma_f32_16x16x32_bf16 v[60:63], v[168:171], v[212:215], v[60:63]
	v_mfma_f32_16x16x32_bf16 v[64:67], v[176:179], v[212:215], v[64:67]
	v_mfma_f32_16x16x32_bf16 v[48:51], v[168:171], v[224:227], v[48:51]
	v_mfma_f32_16x16x32_bf16 v[52:55], v[176:179], v[224:227], v[52:55]
	v_mfma_f32_16x16x32_bf16 v[32:35], v[168:171], v[232:235], v[32:35]
	v_mfma_f32_16x16x32_bf16 v[40:43], v[176:179], v[232:235], v[40:43]
	v_mfma_f32_16x16x32_bf16 v[72:75], v[172:175], v[190:193], v[72:75]
	v_mfma_f32_16x16x32_bf16 v[80:83], v[180:183], v[190:193], v[80:83]
	v_mfma_f32_16x16x32_bf16 v[60:63], v[172:175], v[216:219], v[60:63]
	v_mfma_f32_16x16x32_bf16 v[64:67], v[180:183], v[216:219], v[64:67]
	v_mfma_f32_16x16x32_bf16 v[48:51], v[172:175], v[228:231], v[48:51]
	v_mfma_f32_16x16x32_bf16 v[52:55], v[180:183], v[228:231], v[52:55]
	v_mfma_f32_16x16x32_bf16 v[32:35], v[172:175], v[236:239], v[32:35]
	v_mfma_f32_16x16x32_bf16 v[40:43], v[180:183], v[236:239], v[40:43]
	s_setprio 0
	s_barrier
	s_add_i32 s2, 0, 0x18000
	v_add_u32_e32 v155, s2, v148
	s_add_i32 s54, 0, 0x1c000
	ds_read_b128 v[150:153], v155
	ds_read_b128 v[156:159], v155 offset:1024
	ds_read_b128 v[160:163], v155 offset:2048
	ds_read_b128 v[164:167], v155 offset:3072
	v_add_u32_e32 v155, s54, v148
	ds_read_b128 v[168:171], v155
	ds_read_b128 v[172:175], v155 offset:1024
	ds_read_b128 v[176:179], v155 offset:2048
	ds_read_b128 v[180:183], v155 offset:3072
	s_mov_b32 m0, s17
	v_lshl_add_u64 v[246:247], s[50:51], 0, v[138:139]
	ds_read_b128 v[184:187], v149 offset:32768
	ds_read_b128 v[190:193], v149 offset:33792
	ds_read_b128 v[212:215], v149 offset:34816
	ds_read_b128 v[216:219], v149 offset:35840
	ds_read_b128 v[224:227], v149 offset:36864
	ds_read_b128 v[228:231], v149 offset:37888
	ds_read_b128 v[232:235], v149 offset:38912
	ds_read_b128 v[236:239], v149 offset:39936
	global_load_lds_dwordx4 v[246:247], off
	v_lshl_add_u64 v[246:247], s[50:51], 0, v[140:141]
	s_mov_b32 m0, s18
	s_nop 0
	global_load_lds_dwordx4 v[246:247], off
	s_waitcnt vmcnt(8)
	s_waitcnt lgkmcnt(0)
	s_barrier
	s_setprio 1
	s_waitcnt lgkmcnt(0)
	v_mfma_f32_16x16x32_bf16 v[128:131], v[150:153], v[184:187], v[128:131]
	v_mfma_f32_16x16x32_bf16 v[124:127], v[160:163], v[184:187], v[124:127]
	v_mfma_f32_16x16x32_bf16 v[120:123], v[150:153], v[212:215], v[120:123]
	v_mfma_f32_16x16x32_bf16 v[116:119], v[160:163], v[212:215], v[116:119]
	v_mfma_f32_16x16x32_bf16 v[104:107], v[150:153], v[224:227], v[104:107]
	v_mfma_f32_16x16x32_bf16 v[100:103], v[160:163], v[224:227], v[100:103]
	v_mfma_f32_16x16x32_bf16 v[88:91], v[150:153], v[232:235], v[88:91]
	v_mfma_f32_16x16x32_bf16 v[84:87], v[160:163], v[232:235], v[84:87]
	v_mfma_f32_16x16x32_bf16 v[128:131], v[156:159], v[190:193], v[128:131]
	v_mfma_f32_16x16x32_bf16 v[124:127], v[164:167], v[190:193], v[124:127]
	v_mfma_f32_16x16x32_bf16 v[120:123], v[156:159], v[216:219], v[120:123]
	v_mfma_f32_16x16x32_bf16 v[116:119], v[164:167], v[216:219], v[116:119]
	v_mfma_f32_16x16x32_bf16 v[104:107], v[156:159], v[228:231], v[104:107]
	v_mfma_f32_16x16x32_bf16 v[100:103], v[164:167], v[228:231], v[100:103]
	v_mfma_f32_16x16x32_bf16 v[88:91], v[156:159], v[236:239], v[88:91]
	v_mfma_f32_16x16x32_bf16 v[84:87], v[164:167], v[236:239], v[84:87]
	v_mfma_f32_16x16x32_bf16 v[112:115], v[168:171], v[184:187], v[112:115]
	v_mfma_f32_16x16x32_bf16 v[108:111], v[176:179], v[184:187], v[108:111]
	v_mfma_f32_16x16x32_bf16 v[96:99], v[168:171], v[212:215], v[96:99]
	v_mfma_f32_16x16x32_bf16 v[92:95], v[176:179], v[212:215], v[92:95]
	v_mfma_f32_16x16x32_bf16 v[76:79], v[168:171], v[224:227], v[76:79]
	v_mfma_f32_16x16x32_bf16 v[68:71], v[176:179], v[224:227], v[68:71]
	v_mfma_f32_16x16x32_bf16 v[56:59], v[168:171], v[232:235], v[56:59]
	v_mfma_f32_16x16x32_bf16 v[44:47], v[176:179], v[232:235], v[44:47]
	v_mfma_f32_16x16x32_bf16 v[112:115], v[172:175], v[190:193], v[112:115]
	v_mfma_f32_16x16x32_bf16 v[108:111], v[180:183], v[190:193], v[108:111]
	v_mfma_f32_16x16x32_bf16 v[96:99], v[172:175], v[216:219], v[96:99]
	v_mfma_f32_16x16x32_bf16 v[92:95], v[180:183], v[216:219], v[92:95]
	v_mfma_f32_16x16x32_bf16 v[76:79], v[172:175], v[228:231], v[76:79]
	v_mfma_f32_16x16x32_bf16 v[68:71], v[180:183], v[228:231], v[68:71]
	v_mfma_f32_16x16x32_bf16 v[56:59], v[172:175], v[236:239], v[56:59]
	v_mfma_f32_16x16x32_bf16 v[44:47], v[180:183], v[236:239], v[44:47]
	s_setprio 0
	s_barrier
	s_add_i32 s2, s2, s12
	v_lshl_add_u64 v[194:195], v[194:195], 0, s[30:31]
	s_mov_b32 m0, s2
	ds_read_b128 v[184:187], v149 offset:49152
	ds_read_b128 v[190:193], v149 offset:50176
	ds_read_b128 v[212:215], v149 offset:51200
	ds_read_b128 v[216:219], v149 offset:52224
	ds_read_b128 v[224:227], v149 offset:53248
	ds_read_b128 v[228:231], v149 offset:54272
	ds_read_b128 v[232:235], v149 offset:55296
	ds_read_b128 v[236:239], v149 offset:56320
	global_load_lds_dwordx4 v[194:195], off
	s_add_i32 m0, s2, 0x2000
	s_add_u32 s2, s48, 0x20080
	v_lshl_add_u64 v[194:195], v[240:241], 0, s[30:31]
	s_addc_u32 s3, s49, 0
	s_add_i32 s48, s54, s12
	global_load_lds_dwordx4 v[194:195], off
	v_lshl_add_u64 v[194:195], s[2:3], 0, v[2:3]
	s_mov_b32 m0, s48
	s_nop 0
	global_load_lds_dwordx4 v[194:195], off
	v_lshl_add_u64 v[194:195], s[2:3], 0, v[132:133]
	s_add_i32 m0, s48, 0x2000
	s_nop 0
	global_load_lds_dwordx4 v[194:195], off
	v_lshl_add_u64 v[194:195], v[242:243], 0, s[30:31]
	s_mov_b32 m0, s19
	s_nop 0
	global_load_lds_dwordx4 v[194:195], off
	v_lshl_add_u64 v[194:195], v[244:245], 0, s[30:31]
	s_mov_b32 m0, s20
	s_nop 0
	global_load_lds_dwordx4 v[194:195], off
	s_waitcnt vmcnt(8)
	s_waitcnt lgkmcnt(0)
	s_barrier
	s_setprio 1
	s_waitcnt lgkmcnt(0)
	v_mfma_f32_16x16x32_bf16 v[36:39], v[150:153], v[184:187], v[36:39]
	v_mfma_f32_16x16x32_bf16 v[28:31], v[160:163], v[184:187], v[28:31]
	v_mfma_f32_16x16x32_bf16 v[24:27], v[150:153], v[212:215], v[24:27]
	v_mfma_f32_16x16x32_bf16 v[20:23], v[160:163], v[212:215], v[20:23]
	v_mfma_f32_16x16x32_bf16 v[16:19], v[150:153], v[224:227], v[16:19]
	v_mfma_f32_16x16x32_bf16 v[12:15], v[160:163], v[224:227], v[12:15]
	v_mfma_f32_16x16x32_bf16 v[8:11], v[150:153], v[232:235], v[8:11]
	v_mfma_f32_16x16x32_bf16 v[4:7], v[160:163], v[232:235], v[4:7]
	v_mfma_f32_16x16x32_bf16 v[36:39], v[156:159], v[190:193], v[36:39]
	v_mfma_f32_16x16x32_bf16 v[28:31], v[164:167], v[190:193], v[28:31]
	v_mfma_f32_16x16x32_bf16 v[24:27], v[156:159], v[216:219], v[24:27]
	v_mfma_f32_16x16x32_bf16 v[20:23], v[164:167], v[216:219], v[20:23]
	v_mfma_f32_16x16x32_bf16 v[16:19], v[156:159], v[228:231], v[16:19]
	v_mfma_f32_16x16x32_bf16 v[12:15], v[164:167], v[228:231], v[12:15]
	v_mfma_f32_16x16x32_bf16 v[8:11], v[156:159], v[236:239], v[8:11]
	v_mfma_f32_16x16x32_bf16 v[4:7], v[164:167], v[236:239], v[4:7]
	v_mfma_f32_16x16x32_bf16 v[72:75], v[168:171], v[184:187], v[72:75]
	v_mfma_f32_16x16x32_bf16 v[80:83], v[176:179], v[184:187], v[80:83]
	v_mfma_f32_16x16x32_bf16 v[60:63], v[168:171], v[212:215], v[60:63]
	v_mfma_f32_16x16x32_bf16 v[64:67], v[176:179], v[212:215], v[64:67]
	v_mfma_f32_16x16x32_bf16 v[48:51], v[168:171], v[224:227], v[48:51]
	v_mfma_f32_16x16x32_bf16 v[52:55], v[176:179], v[224:227], v[52:55]
	v_mfma_f32_16x16x32_bf16 v[32:35], v[168:171], v[232:235], v[32:35]
	v_mfma_f32_16x16x32_bf16 v[40:43], v[176:179], v[232:235], v[40:43]
	v_mfma_f32_16x16x32_bf16 v[72:75], v[172:175], v[190:193], v[72:75]
	v_mfma_f32_16x16x32_bf16 v[80:83], v[180:183], v[190:193], v[80:83]
	v_mfma_f32_16x16x32_bf16 v[60:63], v[172:175], v[216:219], v[60:63]
	v_mfma_f32_16x16x32_bf16 v[64:67], v[180:183], v[216:219], v[64:67]
	v_mfma_f32_16x16x32_bf16 v[48:51], v[172:175], v[228:231], v[48:51]
	v_mfma_f32_16x16x32_bf16 v[52:55], v[180:183], v[228:231], v[52:55]
	v_mfma_f32_16x16x32_bf16 v[32:35], v[172:175], v[236:239], v[32:35]
	v_mfma_f32_16x16x32_bf16 v[40:43], v[180:183], v[236:239], v[40:43]
	s_setprio 0
	s_barrier
	s_add_i32 s53, s53, 2
	s_add_u32 s46, s46, 0x100
	s_addc_u32 s47, s47, 0
	s_add_u32 s29, s29, 0x100
	s_addc_u32 s52, s52, 0
	s_cmp_gt_u32 s53, 5
	s_cbranch_scc0 .LBB0_1295
	s_and_b64 vcc, exec, s[38:39]
	v_readlane_b32 s26, v254, 28
	v_readlane_b32 s27, v254, 29
	s_cbranch_vccz .LBB0_1298
	s_barrier

.LBB0_1319:
	s_add_u32 s2, s46, 0x80
	s_addc_u32 s3, s47, 0
	s_cmp_eq_u32 s58, 60
	s_cselect_b32 s51, s52, s3
	s_cselect_b32 s50, s53, s2
	s_cselect_b32 s49, s54, s57
	s_cselect_b32 s48, s55, s56
	s_add_i32 s2, 0, 0x10000
	v_add_u32_e32 v2, s2, v157
	s_add_i32 s59, 0, 0x14000
	ds_read_b128 v[148:151], v2
	ds_read_b128 v[160:163], v2 offset:1024
	ds_read_b128 v[164:167], v2 offset:2048
	ds_read_b128 v[168:171], v2 offset:3072
	v_add_u32_e32 v2, s59, v157
	ds_read_b128 v[172:175], v2
	ds_read_b128 v[176:179], v2 offset:1024
	ds_read_b128 v[180:183], v2 offset:2048
	ds_read_b128 v[184:187], v2 offset:3072
	v_lshl_add_u64 v[152:153], s[46:47], 0, v[146:147]
	s_add_i32 m0, s17, 0xc000
	ds_read_b128 v[190:193], v158
	ds_read_b128 v[212:215], v158 offset:1024
	ds_read_b128 v[216:219], v158 offset:2048
	ds_read_b128 v[224:227], v158 offset:3072
	ds_read_b128 v[228:231], v158 offset:4096
	ds_read_b128 v[232:235], v158 offset:5120
	ds_read_b128 v[236:239], v158 offset:6144
	ds_read_b128 v[240:243], v158 offset:7168
	global_load_lds_dwordx4 v[152:153], off
	v_lshl_add_u64 v[152:153], s[46:47], 0, v[144:145]
	s_add_i32 m0, s17, 0xe000
	s_nop 0
	global_load_lds_dwordx4 v[152:153], off
	s_waitcnt vmcnt(8)
	s_waitcnt lgkmcnt(0)
	s_barrier
	s_setprio 1
	s_waitcnt lgkmcnt(0)
	v_mfma_f32_16x16x32_bf16 v[128:131], v[148:151], v[190:193], v[128:131]
	v_mfma_f32_16x16x32_bf16 v[124:127], v[164:167], v[190:193], v[124:127]
	v_mfma_f32_16x16x32_bf16 v[112:115], v[148:151], v[216:219], v[112:115]
	v_mfma_f32_16x16x32_bf16 v[108:111], v[164:167], v[216:219], v[108:111]
	v_mfma_f32_16x16x32_bf16 v[96:99], v[148:151], v[228:231], v[96:99]
	v_mfma_f32_16x16x32_bf16 v[92:95], v[164:167], v[228:231], v[92:95]
	v_mfma_f32_16x16x32_bf16 v[80:83], v[148:151], v[236:239], v[80:83]
	v_mfma_f32_16x16x32_bf16 v[76:79], v[164:167], v[236:239], v[76:79]
	v_mfma_f32_16x16x32_bf16 v[128:131], v[160:163], v[212:215], v[128:131]
	v_mfma_f32_16x16x32_bf16 v[124:127], v[168:171], v[212:215], v[124:127]
	v_mfma_f32_16x16x32_bf16 v[112:115], v[160:163], v[224:227], v[112:115]
	v_mfma_f32_16x16x32_bf16 v[108:111], v[168:171], v[224:227], v[108:111]
	v_mfma_f32_16x16x32_bf16 v[96:99], v[160:163], v[232:235], v[96:99]
	v_mfma_f32_16x16x32_bf16 v[92:95], v[168:171], v[232:235], v[92:95]
	v_mfma_f32_16x16x32_bf16 v[80:83], v[160:163], v[240:243], v[80:83]
	v_mfma_f32_16x16x32_bf16 v[76:79], v[168:171], v[240:243], v[76:79]
	v_mfma_f32_16x16x32_bf16 v[120:123], v[172:175], v[190:193], v[120:123]
	v_mfma_f32_16x16x32_bf16 v[116:119], v[180:183], v[190:193], v[116:119]
	v_mfma_f32_16x16x32_bf16 v[104:107], v[172:175], v[216:219], v[104:107]
	v_mfma_f32_16x16x32_bf16 v[100:103], v[180:183], v[216:219], v[100:103]
	v_mfma_f32_16x16x32_bf16 v[88:91], v[172:175], v[228:231], v[88:91]
	v_mfma_f32_16x16x32_bf16 v[84:87], v[180:183], v[228:231], v[84:87]
	v_mfma_f32_16x16x32_bf16 v[72:75], v[172:175], v[236:239], v[72:75]
	v_mfma_f32_16x16x32_bf16 v[68:71], v[180:183], v[236:239], v[68:71]
	v_mfma_f32_16x16x32_bf16 v[120:123], v[176:179], v[212:215], v[120:123]
	v_mfma_f32_16x16x32_bf16 v[116:119], v[184:187], v[212:215], v[116:119]
	v_mfma_f32_16x16x32_bf16 v[104:107], v[176:179], v[224:227], v[104:107]
	v_mfma_f32_16x16x32_bf16 v[100:103], v[184:187], v[224:227], v[100:103]
	v_mfma_f32_16x16x32_bf16 v[88:91], v[176:179], v[232:235], v[88:91]
	v_mfma_f32_16x16x32_bf16 v[84:87], v[184:187], v[232:235], v[84:87]
	v_mfma_f32_16x16x32_bf16 v[72:75], v[176:179], v[240:243], v[72:75]
	v_mfma_f32_16x16x32_bf16 v[68:71], v[184:187], v[240:243], v[68:71]
	s_setprio 0
	s_barrier
	s_add_i32 s2, s2, s16
	v_lshl_add_u64 v[152:153], s[48:49], 0, v[132:133]
	s_mov_b32 m0, s2
	ds_read_b128 v[190:193], v158 offset:16384
	ds_read_b128 v[212:215], v158 offset:17408
	ds_read_b128 v[216:219], v158 offset:18432
	ds_read_b128 v[224:227], v158 offset:19456
	ds_read_b128 v[228:231], v158 offset:20480
	ds_read_b128 v[232:235], v158 offset:21504
	ds_read_b128 v[236:239], v158 offset:22528
	ds_read_b128 v[240:243], v158 offset:23552
	global_load_lds_dwordx4 v[152:153], off
	s_add_i32 m0, s2, 0x2000
	s_add_u32 s2, s48, 0x100000
	v_lshl_add_u64 v[194:195], s[48:49], 0, v[134:135]
	s_addc_u32 s3, s49, 0
	s_add_i32 s59, s59, s16
	global_load_lds_dwordx4 v[194:195], off
	v_lshl_add_u64 v[244:245], s[2:3], 0, v[132:133]
	s_mov_b32 m0, s59
	v_lshl_add_u64 v[246:247], s[50:51], 0, v[138:139]
	global_load_lds_dwordx4 v[244:245], off
	v_lshl_add_u64 v[244:245], s[2:3], 0, v[134:135]
	s_add_i32 m0, s59, 0x2000
	s_nop 0
	global_load_lds_dwordx4 v[244:245], off
	v_lshl_add_u64 v[244:245], s[50:51], 0, v[136:137]
	s_mov_b32 m0, s17
	s_nop 0
	global_load_lds_dwordx4 v[244:245], off
	s_mov_b32 m0, s18
	s_nop 0
	global_load_lds_dwordx4 v[246:247], off
	s_waitcnt vmcnt(8)
	s_waitcnt lgkmcnt(0)
	s_barrier
	s_setprio 1
	s_waitcnt lgkmcnt(0)
	v_mfma_f32_16x16x32_bf16 v[56:59], v[148:151], v[190:193], v[56:59]
	v_mfma_f32_16x16x32_bf16 v[52:55], v[164:167], v[190:193], v[52:55]
	v_mfma_f32_16x16x32_bf16 v[40:43], v[148:151], v[216:219], v[40:43]
	v_mfma_f32_16x16x32_bf16 v[36:39], v[164:167], v[216:219], v[36:39]
	v_mfma_f32_16x16x32_bf16 v[24:27], v[148:151], v[228:231], v[24:27]
	v_mfma_f32_16x16x32_bf16 v[20:23], v[164:167], v[228:231], v[20:23]
	v_mfma_f32_16x16x32_bf16 v[8:11], v[148:151], v[236:239], v[8:11]
	v_mfma_f32_16x16x32_bf16 v[4:7], v[164:167], v[236:239], v[4:7]
	v_mfma_f32_16x16x32_bf16 v[56:59], v[160:163], v[212:215], v[56:59]
	v_mfma_f32_16x16x32_bf16 v[52:55], v[168:171], v[212:215], v[52:55]
	v_mfma_f32_16x16x32_bf16 v[40:43], v[160:163], v[224:227], v[40:43]
	v_mfma_f32_16x16x32_bf16 v[36:39], v[168:171], v[224:227], v[36:39]
	v_mfma_f32_16x16x32_bf16 v[24:27], v[160:163], v[232:235], v[24:27]
	v_mfma_f32_16x16x32_bf16 v[20:23], v[168:171], v[232:235], v[20:23]
	v_mfma_f32_16x16x32_bf16 v[8:11], v[160:163], v[240:243], v[8:11]
	v_mfma_f32_16x16x32_bf16 v[4:7], v[168:171], v[240:243], v[4:7]
	v_mfma_f32_16x16x32_bf16 v[60:63], v[172:175], v[190:193], v[60:63]
	v_mfma_f32_16x16x32_bf16 v[64:67], v[180:183], v[190:193], v[64:67]
	v_mfma_f32_16x16x32_bf16 v[44:47], v[172:175], v[216:219], v[44:47]
	v_mfma_f32_16x16x32_bf16 v[48:51], v[180:183], v[216:219], v[48:51]
	v_mfma_f32_16x16x32_bf16 v[28:31], v[172:175], v[228:231], v[28:31]
	v_mfma_f32_16x16x32_bf16 v[32:35], v[180:183], v[228:231], v[32:35]
	v_mfma_f32_16x16x32_bf16 v[12:15], v[172:175], v[236:239], v[12:15]
	v_mfma_f32_16x16x32_bf16 v[16:19], v[180:183], v[236:239], v[16:19]
	v_mfma_f32_16x16x32_bf16 v[60:63], v[176:179], v[212:215], v[60:63]
	v_mfma_f32_16x16x32_bf16 v[64:67], v[184:187], v[212:215], v[64:67]
	v_mfma_f32_16x16x32_bf16 v[44:47], v[176:179], v[224:227], v[44:47]
	v_mfma_f32_16x16x32_bf16 v[48:51], v[184:187], v[224:227], v[48:51]
	v_mfma_f32_16x16x32_bf16 v[28:31], v[176:179], v[232:235], v[28:31]
	v_mfma_f32_16x16x32_bf16 v[32:35], v[184:187], v[232:235], v[32:35]
	v_mfma_f32_16x16x32_bf16 v[12:15], v[176:179], v[240:243], v[12:15]
	v_mfma_f32_16x16x32_bf16 v[16:19], v[184:187], v[240:243], v[16:19]
	s_setprio 0
	s_barrier
	s_add_i32 s2, 0, 0x18000
	v_add_u32_e32 v2, s2, v157
	s_add_i32 s59, 0, 0x1c000
	ds_read_b128 v[148:151], v2
	ds_read_b128 v[160:163], v2 offset:1024
	ds_read_b128 v[164:167], v2 offset:2048
	ds_read_b128 v[168:171], v2 offset:3072
	v_add_u32_e32 v2, s59, v157
	ds_read_b128 v[172:175], v2
	ds_read_b128 v[176:179], v2 offset:1024
	ds_read_b128 v[180:183], v2 offset:2048
	ds_read_b128 v[184:187], v2 offset:3072
	s_mov_b32 m0, s19
	v_lshl_add_u64 v[248:249], s[50:51], 0, v[140:141]
	ds_read_b128 v[190:193], v158 offset:32768
	ds_read_b128 v[212:215], v158 offset:33792
	ds_read_b128 v[216:219], v158 offset:34816
	ds_read_b128 v[224:227], v158 offset:35840
	ds_read_b128 v[228:231], v158 offset:36864
	ds_read_b128 v[232:235], v158 offset:37888
	ds_read_b128 v[236:239], v158 offset:38912
	ds_read_b128 v[240:243], v158 offset:39936
	global_load_lds_dwordx4 v[248:249], off
	v_lshl_add_u64 v[248:249], s[50:51], 0, v[142:143]
	s_mov_b32 m0, s20
	s_nop 0
	global_load_lds_dwordx4 v[248:249], off
	s_waitcnt vmcnt(8)
	s_waitcnt lgkmcnt(0)
	s_barrier
	s_setprio 1
	s_waitcnt lgkmcnt(0)
	v_mfma_f32_16x16x32_bf16 v[128:131], v[148:151], v[190:193], v[128:131]
	v_mfma_f32_16x16x32_bf16 v[124:127], v[164:167], v[190:193], v[124:127]
	v_mfma_f32_16x16x32_bf16 v[112:115], v[148:151], v[216:219], v[112:115]
	v_mfma_f32_16x16x32_bf16 v[108:111], v[164:167], v[216:219], v[108:111]
	v_mfma_f32_16x16x32_bf16 v[96:99], v[148:151], v[228:231], v[96:99]
	v_mfma_f32_16x16x32_bf16 v[92:95], v[164:167], v[228:231], v[92:95]
	v_mfma_f32_16x16x32_bf16 v[80:83], v[148:151], v[236:239], v[80:83]
	v_mfma_f32_16x16x32_bf16 v[76:79], v[164:167], v[236:239], v[76:79]
	v_mfma_f32_16x16x32_bf16 v[128:131], v[160:163], v[212:215], v[128:131]
	v_mfma_f32_16x16x32_bf16 v[124:127], v[168:171], v[212:215], v[124:127]
	v_mfma_f32_16x16x32_bf16 v[112:115], v[160:163], v[224:227], v[112:115]
	v_mfma_f32_16x16x32_bf16 v[108:111], v[168:171], v[224:227], v[108:111]
	v_mfma_f32_16x16x32_bf16 v[96:99], v[160:163], v[232:235], v[96:99]
	v_mfma_f32_16x16x32_bf16 v[92:95], v[168:171], v[232:235], v[92:95]
	v_mfma_f32_16x16x32_bf16 v[80:83], v[160:163], v[240:243], v[80:83]
	v_mfma_f32_16x16x32_bf16 v[76:79], v[168:171], v[240:243], v[76:79]
	v_mfma_f32_16x16x32_bf16 v[120:123], v[172:175], v[190:193], v[120:123]
	v_mfma_f32_16x16x32_bf16 v[116:119], v[180:183], v[190:193], v[116:119]
	v_mfma_f32_16x16x32_bf16 v[104:107], v[172:175], v[216:219], v[104:107]
	v_mfma_f32_16x16x32_bf16 v[100:103], v[180:183], v[216:219], v[100:103]
	v_mfma_f32_16x16x32_bf16 v[88:91], v[172:175], v[228:231], v[88:91]
	v_mfma_f32_16x16x32_bf16 v[84:87], v[180:183], v[228:231], v[84:87]
	v_mfma_f32_16x16x32_bf16 v[72:75], v[172:175], v[236:239], v[72:75]
	v_mfma_f32_16x16x32_bf16 v[68:71], v[180:183], v[236:239], v[68:71]
	v_mfma_f32_16x16x32_bf16 v[120:123], v[176:179], v[212:215], v[120:123]
	v_mfma_f32_16x16x32_bf16 v[116:119], v[184:187], v[212:215], v[116:119]
	v_mfma_f32_16x16x32_bf16 v[104:107], v[176:179], v[224:227], v[104:107]
	v_mfma_f32_16x16x32_bf16 v[100:103], v[184:187], v[224:227], v[100:103]
	v_mfma_f32_16x16x32_bf16 v[88:91], v[176:179], v[232:235], v[88:91]
	v_mfma_f32_16x16x32_bf16 v[84:87], v[184:187], v[232:235], v[84:87]
	v_mfma_f32_16x16x32_bf16 v[72:75], v[176:179], v[240:243], v[72:75]
	v_mfma_f32_16x16x32_bf16 v[68:71], v[184:187], v[240:243], v[68:71]
	s_setprio 0
	s_barrier
	s_add_i32 s2, s2, s16
	v_lshl_add_u64 v[152:153], v[152:153], 0, s[30:31]
	s_mov_b32 m0, s2
	ds_read_b128 v[190:193], v158 offset:49152
	ds_read_b128 v[212:215], v158 offset:50176
	ds_read_b128 v[216:219], v158 offset:51200
	ds_read_b128 v[224:227], v158 offset:52224
	ds_read_b128 v[228:231], v158 offset:53248
	ds_read_b128 v[232:235], v158 offset:54272
	ds_read_b128 v[236:239], v158 offset:55296
	ds_read_b128 v[240:243], v158 offset:56320
	global_load_lds_dwordx4 v[152:153], off
	s_add_i32 m0, s2, 0x2000
	s_add_u32 s2, s48, 0x100080
	v_lshl_add_u64 v[152:153], v[194:195], 0, s[30:31]
	s_addc_u32 s3, s49, 0
	s_add_i32 s48, s59, s16
	global_load_lds_dwordx4 v[152:153], off
	v_lshl_add_u64 v[152:153], s[2:3], 0, v[132:133]
	s_mov_b32 m0, s48
	s_nop 0
	global_load_lds_dwordx4 v[152:153], off
	v_lshl_add_u64 v[152:153], s[2:3], 0, v[134:135]
	s_add_i32 m0, s48, 0x2000
	s_nop 0
	global_load_lds_dwordx4 v[152:153], off
	v_lshl_add_u64 v[152:153], v[244:245], 0, s[30:31]
	s_mov_b32 m0, s23
	s_nop 0
	global_load_lds_dwordx4 v[152:153], off
	v_lshl_add_u64 v[152:153], v[246:247], 0, s[30:31]
	s_mov_b32 m0, s24
	s_nop 0
	global_load_lds_dwordx4 v[152:153], off
	s_waitcnt vmcnt(8)
	s_waitcnt lgkmcnt(0)
	s_barrier
	s_setprio 1
	s_waitcnt lgkmcnt(0)
	v_mfma_f32_16x16x32_bf16 v[56:59], v[148:151], v[190:193], v[56:59]
	v_mfma_f32_16x16x32_bf16 v[52:55], v[164:167], v[190:193], v[52:55]
	v_mfma_f32_16x16x32_bf16 v[40:43], v[148:151], v[216:219], v[40:43]
	v_mfma_f32_16x16x32_bf16 v[36:39], v[164:167], v[216:219], v[36:39]
	v_mfma_f32_16x16x32_bf16 v[24:27], v[148:151], v[228:231], v[24:27]
	v_mfma_f32_16x16x32_bf16 v[20:23], v[164:167], v[228:231], v[20:23]
	v_mfma_f32_16x16x32_bf16 v[8:11], v[148:151], v[236:239], v[8:11]
	v_mfma_f32_16x16x32_bf16 v[4:7], v[164:167], v[236:239], v[4:7]
	v_mfma_f32_16x16x32_bf16 v[56:59], v[160:163], v[212:215], v[56:59]
	v_mfma_f32_16x16x32_bf16 v[52:55], v[168:171], v[212:215], v[52:55]
	v_mfma_f32_16x16x32_bf16 v[40:43], v[160:163], v[224:227], v[40:43]
	v_mfma_f32_16x16x32_bf16 v[36:39], v[168:171], v[224:227], v[36:39]
	v_mfma_f32_16x16x32_bf16 v[24:27], v[160:163], v[232:235], v[24:27]
	v_mfma_f32_16x16x32_bf16 v[20:23], v[168:171], v[232:235], v[20:23]
	v_mfma_f32_16x16x32_bf16 v[8:11], v[160:163], v[240:243], v[8:11]
	v_mfma_f32_16x16x32_bf16 v[4:7], v[168:171], v[240:243], v[4:7]
	v_mfma_f32_16x16x32_bf16 v[60:63], v[172:175], v[190:193], v[60:63]
	v_mfma_f32_16x16x32_bf16 v[64:67], v[180:183], v[190:193], v[64:67]
	v_mfma_f32_16x16x32_bf16 v[44:47], v[172:175], v[216:219], v[44:47]
	v_mfma_f32_16x16x32_bf16 v[48:51], v[180:183], v[216:219], v[48:51]
	v_mfma_f32_16x16x32_bf16 v[28:31], v[172:175], v[228:231], v[28:31]
	v_mfma_f32_16x16x32_bf16 v[32:35], v[180:183], v[228:231], v[32:35]
	v_mfma_f32_16x16x32_bf16 v[12:15], v[172:175], v[236:239], v[12:15]
	v_mfma_f32_16x16x32_bf16 v[16:19], v[180:183], v[236:239], v[16:19]
	v_mfma_f32_16x16x32_bf16 v[60:63], v[176:179], v[212:215], v[60:63]
	v_mfma_f32_16x16x32_bf16 v[64:67], v[184:187], v[212:215], v[64:67]
	v_mfma_f32_16x16x32_bf16 v[44:47], v[176:179], v[224:227], v[44:47]
	v_mfma_f32_16x16x32_bf16 v[48:51], v[184:187], v[224:227], v[48:51]
	v_mfma_f32_16x16x32_bf16 v[28:31], v[176:179], v[232:235], v[28:31]
	v_mfma_f32_16x16x32_bf16 v[32:35], v[184:187], v[232:235], v[32:35]
	v_mfma_f32_16x16x32_bf16 v[12:15], v[176:179], v[240:243], v[12:15]
	v_mfma_f32_16x16x32_bf16 v[16:19], v[184:187], v[240:243], v[16:19]
	s_setprio 0
	s_barrier
	s_add_i32 s58, s58, 2
	s_add_u32 s46, s46, 0x100
	s_addc_u32 s47, s47, 0
	s_add_u32 s56, s56, 0x100
	s_addc_u32 s57, s57, 0
	s_cmp_gt_u32 s58, 61
	s_cbranch_scc0 .LBB0_1319
	s_and_b64 vcc, exec, s[36:37]
	s_cbranch_vccz .LBB0_1322
	s_barrier

.LBB0_2022:
	s_add_u32 s2, s56, 0x80
	s_addc_u32 s3, s57, 0
	s_cmp_eq_u32 s43, 28
	s_cselect_b32 s61, s49, s3
	s_cselect_b32 s60, s48, s2
	s_cselect_b32 s59, s51, s7
	s_cselect_b32 s58, s50, s6
	s_add_i32 s2, 0, 0x10000
	v_add_u32_e32 v2, s2, v214
	s_add_i32 s47, 0, 0x14000
	s_waitcnt vmcnt(0)
	ds_read_b128 v[120:123], v2
	ds_read_b128 v[128:131], v2 offset:1024
	ds_read_b128 v[132:135], v2 offset:2048
	ds_read_b128 v[136:139], v2 offset:3072
	v_add_u32_e32 v2, s47, v214
	ds_read_b128 v[148:151], v2
	ds_read_b128 v[152:155], v2 offset:1024
	ds_read_b128 v[172:175], v2 offset:2048
	ds_read_b128 v[176:179], v2 offset:3072
	v_lshl_add_u64 v[194:195], s[56:57], 0, v[170:171]
	s_add_i32 m0, s20, 0xc000
	ds_read_b128 v[180:183], v215
	ds_read_b128 v[184:187], v215 offset:1024
	ds_read_b128 v[190:193], v215 offset:2048
	ds_read_b128 v[216:219], v215 offset:3072
	ds_read_b128 v[224:227], v215 offset:4096
	ds_read_b128 v[228:231], v215 offset:5120
	ds_read_b128 v[232:235], v215 offset:6144
	ds_read_b128 v[236:239], v215 offset:7168
	global_load_lds_dwordx4 v[194:195], off
	v_lshl_add_u64 v[194:195], s[56:57], 0, v[168:169]
	s_add_i32 m0, s20, 0xe000
	s_nop 0
	global_load_lds_dwordx4 v[194:195], off
	s_waitcnt vmcnt(8)
	s_waitcnt lgkmcnt(0)
	s_barrier
	s_setprio 1
	s_waitcnt lgkmcnt(0)
	v_mfma_f32_16x16x32_bf16 v[144:147], v[120:123], v[180:183], v[144:147]
	v_mfma_f32_16x16x32_bf16 v[140:143], v[132:135], v[180:183], v[140:143]
	v_mfma_f32_16x16x32_bf16 v[112:115], v[120:123], v[190:193], v[112:115]
	v_mfma_f32_16x16x32_bf16 v[108:111], v[132:135], v[190:193], v[108:111]
	v_mfma_f32_16x16x32_bf16 v[96:99], v[120:123], v[224:227], v[96:99]
	v_mfma_f32_16x16x32_bf16 v[92:95], v[132:135], v[224:227], v[92:95]
	v_mfma_f32_16x16x32_bf16 v[80:83], v[120:123], v[232:235], v[80:83]
	v_mfma_f32_16x16x32_bf16 v[76:79], v[132:135], v[232:235], v[76:79]
	v_mfma_f32_16x16x32_bf16 v[144:147], v[128:131], v[184:187], v[144:147]
	v_mfma_f32_16x16x32_bf16 v[140:143], v[136:139], v[184:187], v[140:143]
	v_mfma_f32_16x16x32_bf16 v[112:115], v[128:131], v[216:219], v[112:115]
	v_mfma_f32_16x16x32_bf16 v[108:111], v[136:139], v[216:219], v[108:111]
	v_mfma_f32_16x16x32_bf16 v[96:99], v[128:131], v[228:231], v[96:99]
	v_mfma_f32_16x16x32_bf16 v[92:95], v[136:139], v[228:231], v[92:95]
	v_mfma_f32_16x16x32_bf16 v[80:83], v[128:131], v[236:239], v[80:83]
	v_mfma_f32_16x16x32_bf16 v[76:79], v[136:139], v[236:239], v[76:79]
	v_mfma_f32_16x16x32_bf16 v[124:127], v[148:151], v[180:183], v[124:127]
	v_mfma_f32_16x16x32_bf16 v[116:119], v[172:175], v[180:183], v[116:119]
	v_mfma_f32_16x16x32_bf16 v[104:107], v[148:151], v[190:193], v[104:107]
	v_mfma_f32_16x16x32_bf16 v[100:103], v[172:175], v[190:193], v[100:103]
	v_mfma_f32_16x16x32_bf16 v[88:91], v[148:151], v[224:227], v[88:91]
	v_mfma_f32_16x16x32_bf16 v[84:87], v[172:175], v[224:227], v[84:87]
	v_mfma_f32_16x16x32_bf16 v[72:75], v[148:151], v[232:235], v[72:75]
	v_mfma_f32_16x16x32_bf16 v[68:71], v[172:175], v[232:235], v[68:71]
	v_mfma_f32_16x16x32_bf16 v[124:127], v[152:155], v[184:187], v[124:127]
	v_mfma_f32_16x16x32_bf16 v[116:119], v[176:179], v[184:187], v[116:119]
	v_mfma_f32_16x16x32_bf16 v[104:107], v[152:155], v[216:219], v[104:107]
	v_mfma_f32_16x16x32_bf16 v[100:103], v[176:179], v[216:219], v[100:103]
	v_mfma_f32_16x16x32_bf16 v[88:91], v[152:155], v[228:231], v[88:91]
	v_mfma_f32_16x16x32_bf16 v[84:87], v[176:179], v[228:231], v[84:87]
	v_mfma_f32_16x16x32_bf16 v[72:75], v[152:155], v[236:239], v[72:75]
	v_mfma_f32_16x16x32_bf16 v[68:71], v[176:179], v[236:239], v[68:71]
	s_setprio 0
	s_barrier
	s_add_i32 s2, s2, s19
	v_lshl_add_u64 v[194:195], s[58:59], 0, v[156:157]
	s_mov_b32 m0, s2
	ds_read_b128 v[180:183], v215 offset:16384
	ds_read_b128 v[184:187], v215 offset:17408
	ds_read_b128 v[190:193], v215 offset:18432
	ds_read_b128 v[216:219], v215 offset:19456
	ds_read_b128 v[224:227], v215 offset:20480
	ds_read_b128 v[228:231], v215 offset:21504
	ds_read_b128 v[232:235], v215 offset:22528
	ds_read_b128 v[236:239], v215 offset:23552
	global_load_lds_dwordx4 v[194:195], off
	s_add_i32 m0, s2, 0x2000
	s_add_u32 s2, s58, 0x80000
	v_lshl_add_u64 v[240:241], s[58:59], 0, v[158:159]
	s_addc_u32 s3, s59, 0
	s_add_i32 s47, s47, s19
	global_load_lds_dwordx4 v[240:241], off
	v_lshl_add_u64 v[242:243], s[2:3], 0, v[156:157]
	s_mov_b32 m0, s47
	v_lshl_add_u64 v[244:245], s[60:61], 0, v[162:163]
	global_load_lds_dwordx4 v[242:243], off
	v_lshl_add_u64 v[242:243], s[2:3], 0, v[158:159]
	s_add_i32 m0, s47, 0x2000
	s_nop 0
	global_load_lds_dwordx4 v[242:243], off
	v_lshl_add_u64 v[242:243], s[60:61], 0, v[160:161]
	s_mov_b32 m0, s20
	s_nop 0
	global_load_lds_dwordx4 v[242:243], off
	s_mov_b32 m0, s21
	s_nop 0
	global_load_lds_dwordx4 v[244:245], off
	s_waitcnt vmcnt(8)
	s_waitcnt lgkmcnt(0)
	s_barrier
	s_setprio 1
	s_waitcnt lgkmcnt(0)
	v_mfma_f32_16x16x32_bf16 v[56:59], v[120:123], v[180:183], v[56:59]
	v_mfma_f32_16x16x32_bf16 v[52:55], v[132:135], v[180:183], v[52:55]
	v_mfma_f32_16x16x32_bf16 v[40:43], v[120:123], v[190:193], v[40:43]
	v_mfma_f32_16x16x32_bf16 v[36:39], v[132:135], v[190:193], v[36:39]
	v_mfma_f32_16x16x32_bf16 v[24:27], v[120:123], v[224:227], v[24:27]
	v_mfma_f32_16x16x32_bf16 v[20:23], v[132:135], v[224:227], v[20:23]
	v_mfma_f32_16x16x32_bf16 v[8:11], v[120:123], v[232:235], v[8:11]
	v_mfma_f32_16x16x32_bf16 v[4:7], v[132:135], v[232:235], v[4:7]
	v_mfma_f32_16x16x32_bf16 v[56:59], v[128:131], v[184:187], v[56:59]
	v_mfma_f32_16x16x32_bf16 v[52:55], v[136:139], v[184:187], v[52:55]
	v_mfma_f32_16x16x32_bf16 v[40:43], v[128:131], v[216:219], v[40:43]
	v_mfma_f32_16x16x32_bf16 v[36:39], v[136:139], v[216:219], v[36:39]
	v_mfma_f32_16x16x32_bf16 v[24:27], v[128:131], v[228:231], v[24:27]
	v_mfma_f32_16x16x32_bf16 v[20:23], v[136:139], v[228:231], v[20:23]
	v_mfma_f32_16x16x32_bf16 v[8:11], v[128:131], v[236:239], v[8:11]
	v_mfma_f32_16x16x32_bf16 v[4:7], v[136:139], v[236:239], v[4:7]
	v_mfma_f32_16x16x32_bf16 v[64:67], v[148:151], v[180:183], v[64:67]
	v_mfma_f32_16x16x32_bf16 v[60:63], v[172:175], v[180:183], v[60:63]
	v_mfma_f32_16x16x32_bf16 v[48:51], v[148:151], v[190:193], v[48:51]
	v_mfma_f32_16x16x32_bf16 v[44:47], v[172:175], v[190:193], v[44:47]
	v_mfma_f32_16x16x32_bf16 v[32:35], v[148:151], v[224:227], v[32:35]
	v_mfma_f32_16x16x32_bf16 v[28:31], v[172:175], v[224:227], v[28:31]
	v_mfma_f32_16x16x32_bf16 v[16:19], v[148:151], v[232:235], v[16:19]
	v_mfma_f32_16x16x32_bf16 v[12:15], v[172:175], v[232:235], v[12:15]
	v_mfma_f32_16x16x32_bf16 v[64:67], v[152:155], v[184:187], v[64:67]
	v_mfma_f32_16x16x32_bf16 v[60:63], v[176:179], v[184:187], v[60:63]
	v_mfma_f32_16x16x32_bf16 v[48:51], v[152:155], v[216:219], v[48:51]
	v_mfma_f32_16x16x32_bf16 v[44:47], v[176:179], v[216:219], v[44:47]
	v_mfma_f32_16x16x32_bf16 v[32:35], v[152:155], v[228:231], v[32:35]
	v_mfma_f32_16x16x32_bf16 v[28:31], v[176:179], v[228:231], v[28:31]
	v_mfma_f32_16x16x32_bf16 v[16:19], v[152:155], v[236:239], v[16:19]
	v_mfma_f32_16x16x32_bf16 v[12:15], v[176:179], v[236:239], v[12:15]
	s_setprio 0
	s_barrier
	s_add_i32 s2, 0, 0x18000
	v_add_u32_e32 v2, s2, v214
	s_add_i32 s47, 0, 0x1c000
	ds_read_b128 v[120:123], v2
	ds_read_b128 v[128:131], v2 offset:1024
	ds_read_b128 v[132:135], v2 offset:2048
	ds_read_b128 v[136:139], v2 offset:3072
	v_add_u32_e32 v2, s47, v214
	ds_read_b128 v[148:151], v2
	ds_read_b128 v[152:155], v2 offset:1024
	ds_read_b128 v[172:175], v2 offset:2048
	ds_read_b128 v[176:179], v2 offset:3072
	s_mov_b32 m0, s22
	v_lshl_add_u64 v[246:247], s[60:61], 0, v[164:165]
	ds_read_b128 v[180:183], v215 offset:32768
	ds_read_b128 v[184:187], v215 offset:33792
	ds_read_b128 v[190:193], v215 offset:34816
	ds_read_b128 v[216:219], v215 offset:35840
	ds_read_b128 v[224:227], v215 offset:36864
	ds_read_b128 v[228:231], v215 offset:37888
	ds_read_b128 v[232:235], v215 offset:38912
	ds_read_b128 v[236:239], v215 offset:39936
	global_load_lds_dwordx4 v[246:247], off
	v_lshl_add_u64 v[246:247], s[60:61], 0, v[166:167]
	s_mov_b32 m0, s23
	s_nop 0
	global_load_lds_dwordx4 v[246:247], off
	s_waitcnt vmcnt(8)
	s_waitcnt lgkmcnt(0)
	s_barrier
	s_setprio 1
	s_waitcnt lgkmcnt(0)
	v_mfma_f32_16x16x32_bf16 v[144:147], v[120:123], v[180:183], v[144:147]
	v_mfma_f32_16x16x32_bf16 v[140:143], v[132:135], v[180:183], v[140:143]
	v_mfma_f32_16x16x32_bf16 v[112:115], v[120:123], v[190:193], v[112:115]
	v_mfma_f32_16x16x32_bf16 v[108:111], v[132:135], v[190:193], v[108:111]
	v_mfma_f32_16x16x32_bf16 v[96:99], v[120:123], v[224:227], v[96:99]
	v_mfma_f32_16x16x32_bf16 v[92:95], v[132:135], v[224:227], v[92:95]
	v_mfma_f32_16x16x32_bf16 v[80:83], v[120:123], v[232:235], v[80:83]
	v_mfma_f32_16x16x32_bf16 v[76:79], v[132:135], v[232:235], v[76:79]
	v_mfma_f32_16x16x32_bf16 v[144:147], v[128:131], v[184:187], v[144:147]
	v_mfma_f32_16x16x32_bf16 v[140:143], v[136:139], v[184:187], v[140:143]
	v_mfma_f32_16x16x32_bf16 v[112:115], v[128:131], v[216:219], v[112:115]
	v_mfma_f32_16x16x32_bf16 v[108:111], v[136:139], v[216:219], v[108:111]
	v_mfma_f32_16x16x32_bf16 v[96:99], v[128:131], v[228:231], v[96:99]
	v_mfma_f32_16x16x32_bf16 v[92:95], v[136:139], v[228:231], v[92:95]
	v_mfma_f32_16x16x32_bf16 v[80:83], v[128:131], v[236:239], v[80:83]
	v_mfma_f32_16x16x32_bf16 v[76:79], v[136:139], v[236:239], v[76:79]
	v_mfma_f32_16x16x32_bf16 v[124:127], v[148:151], v[180:183], v[124:127]
	v_mfma_f32_16x16x32_bf16 v[116:119], v[172:175], v[180:183], v[116:119]
	v_mfma_f32_16x16x32_bf16 v[104:107], v[148:151], v[190:193], v[104:107]
	v_mfma_f32_16x16x32_bf16 v[100:103], v[172:175], v[190:193], v[100:103]
	v_mfma_f32_16x16x32_bf16 v[88:91], v[148:151], v[224:227], v[88:91]
	v_mfma_f32_16x16x32_bf16 v[84:87], v[172:175], v[224:227], v[84:87]
	v_mfma_f32_16x16x32_bf16 v[72:75], v[148:151], v[232:235], v[72:75]
	v_mfma_f32_16x16x32_bf16 v[68:71], v[172:175], v[232:235], v[68:71]
	v_mfma_f32_16x16x32_bf16 v[124:127], v[152:155], v[184:187], v[124:127]
	v_mfma_f32_16x16x32_bf16 v[116:119], v[176:179], v[184:187], v[116:119]
	v_mfma_f32_16x16x32_bf16 v[104:107], v[152:155], v[216:219], v[104:107]
	v_mfma_f32_16x16x32_bf16 v[100:103], v[176:179], v[216:219], v[100:103]
	v_mfma_f32_16x16x32_bf16 v[88:91], v[152:155], v[228:231], v[88:91]
	v_mfma_f32_16x16x32_bf16 v[84:87], v[176:179], v[228:231], v[84:87]
	v_mfma_f32_16x16x32_bf16 v[72:75], v[152:155], v[236:239], v[72:75]
	v_mfma_f32_16x16x32_bf16 v[68:71], v[176:179], v[236:239], v[68:71]
	s_setprio 0
	s_barrier
	s_add_i32 s2, s2, s19
	v_lshl_add_u64 v[194:195], v[194:195], 0, s[30:31]
	s_mov_b32 m0, s2
	ds_read_b128 v[180:183], v215 offset:49152
	ds_read_b128 v[184:187], v215 offset:50176
	ds_read_b128 v[190:193], v215 offset:51200
	ds_read_b128 v[216:219], v215 offset:52224
	ds_read_b128 v[224:227], v215 offset:53248
	ds_read_b128 v[228:231], v215 offset:54272
	ds_read_b128 v[232:235], v215 offset:55296
	ds_read_b128 v[236:239], v215 offset:56320
	global_load_lds_dwordx4 v[194:195], off
	s_add_i32 m0, s2, 0x2000
	s_add_u32 s2, s58, 0x80080
	v_lshl_add_u64 v[194:195], v[240:241], 0, s[30:31]
	s_addc_u32 s3, s59, 0
	s_add_i32 s47, s47, s19
	global_load_lds_dwordx4 v[194:195], off
	v_lshl_add_u64 v[194:195], s[2:3], 0, v[156:157]
	s_mov_b32 m0, s47
	s_nop 0
	global_load_lds_dwordx4 v[194:195], off
	v_lshl_add_u64 v[194:195], s[2:3], 0, v[158:159]
	s_add_i32 m0, s47, 0x2000
	s_nop 0
	global_load_lds_dwordx4 v[194:195], off
	v_lshl_add_u64 v[194:195], v[242:243], 0, s[30:31]
	s_mov_b32 m0, s28
	s_nop 0
	global_load_lds_dwordx4 v[194:195], off
	v_lshl_add_u64 v[194:195], v[244:245], 0, s[30:31]
	s_mov_b32 m0, s29
	s_nop 0
	global_load_lds_dwordx4 v[194:195], off
	s_waitcnt vmcnt(8)
	s_waitcnt lgkmcnt(0)
	s_barrier
	s_setprio 1
	s_waitcnt lgkmcnt(0)
	v_mfma_f32_16x16x32_bf16 v[56:59], v[120:123], v[180:183], v[56:59]
	v_mfma_f32_16x16x32_bf16 v[52:55], v[132:135], v[180:183], v[52:55]
	v_mfma_f32_16x16x32_bf16 v[40:43], v[120:123], v[190:193], v[40:43]
	v_mfma_f32_16x16x32_bf16 v[36:39], v[132:135], v[190:193], v[36:39]
	v_mfma_f32_16x16x32_bf16 v[24:27], v[120:123], v[224:227], v[24:27]
	v_mfma_f32_16x16x32_bf16 v[20:23], v[132:135], v[224:227], v[20:23]
	v_mfma_f32_16x16x32_bf16 v[8:11], v[120:123], v[232:235], v[8:11]
	v_mfma_f32_16x16x32_bf16 v[4:7], v[132:135], v[232:235], v[4:7]
	v_mfma_f32_16x16x32_bf16 v[56:59], v[128:131], v[184:187], v[56:59]
	v_mfma_f32_16x16x32_bf16 v[52:55], v[136:139], v[184:187], v[52:55]
	v_mfma_f32_16x16x32_bf16 v[40:43], v[128:131], v[216:219], v[40:43]
	v_mfma_f32_16x16x32_bf16 v[36:39], v[136:139], v[216:219], v[36:39]
	v_mfma_f32_16x16x32_bf16 v[24:27], v[128:131], v[228:231], v[24:27]
	v_mfma_f32_16x16x32_bf16 v[20:23], v[136:139], v[228:231], v[20:23]
	v_mfma_f32_16x16x32_bf16 v[8:11], v[128:131], v[236:239], v[8:11]
	v_mfma_f32_16x16x32_bf16 v[4:7], v[136:139], v[236:239], v[4:7]
	v_mfma_f32_16x16x32_bf16 v[64:67], v[148:151], v[180:183], v[64:67]
	v_mfma_f32_16x16x32_bf16 v[60:63], v[172:175], v[180:183], v[60:63]
	v_mfma_f32_16x16x32_bf16 v[48:51], v[148:151], v[190:193], v[48:51]
	v_mfma_f32_16x16x32_bf16 v[44:47], v[172:175], v[190:193], v[44:47]
	v_mfma_f32_16x16x32_bf16 v[32:35], v[148:151], v[224:227], v[32:35]
	v_mfma_f32_16x16x32_bf16 v[28:31], v[172:175], v[224:227], v[28:31]
	v_mfma_f32_16x16x32_bf16 v[16:19], v[148:151], v[232:235], v[16:19]
	v_mfma_f32_16x16x32_bf16 v[12:15], v[172:175], v[232:235], v[12:15]
	v_mfma_f32_16x16x32_bf16 v[64:67], v[152:155], v[184:187], v[64:67]
	v_mfma_f32_16x16x32_bf16 v[60:63], v[176:179], v[184:187], v[60:63]
	v_mfma_f32_16x16x32_bf16 v[48:51], v[152:155], v[216:219], v[48:51]
	v_mfma_f32_16x16x32_bf16 v[44:47], v[176:179], v[216:219], v[44:47]
	v_mfma_f32_16x16x32_bf16 v[32:35], v[152:155], v[228:231], v[32:35]
	v_mfma_f32_16x16x32_bf16 v[28:31], v[176:179], v[228:231], v[28:31]
	v_mfma_f32_16x16x32_bf16 v[16:19], v[152:155], v[236:239], v[16:19]
	v_mfma_f32_16x16x32_bf16 v[12:15], v[176:179], v[236:239], v[12:15]
	s_setprio 0
	s_barrier
	s_add_i32 s43, s43, 2
	s_add_u32 s56, s56, 0x100
	s_addc_u32 s57, s57, 0
	s_add_u32 s6, s6, 0x100
	s_addc_u32 s7, s7, 0
	s_cmp_gt_u32 s43, 29
	s_cbranch_scc0 .LBB0_2022
	s_and_b64 vcc, exec, s[40:41]
	s_cbranch_vccz .LBB0_2025
	s_barrier

.LBB0_2360:
	s_add_u32 s2, s0, s56
	s_addc_u32 s3, s1, s57
	s_add_u32 s53, s2, 0x40200100
	s_addc_u32 s55, s3, 0
	s_add_u32 s58, s7, s56
	s_addc_u32 s59, s47, s57
	s_cmpk_eq_i32 s56, 0xf00
	s_cselect_b64 vcc, -1, 0
	s_and_b64 s[2:3], vcc, exec
	s_cselect_b32 s61, s37, s55
	s_cselect_b32 s60, s36, s53
	s_cselect_b32 s59, s51, s59
	s_cselect_b32 s58, s50, s58
	s_add_i32 s2, 0, 0x10000
	s_add_i32 s53, 0, 0x14000
	v_add_u32_e32 v170, s2, v154
	v_add_u32_e32 v187, s53, v154
	ds_read_b128 v[158:161], v170
	ds_read_b128 v[162:165], v170 offset:1024
	ds_read_b128 v[166:169], v170 offset:2048
	ds_read_b128 v[170:173], v170 offset:3072
	ds_read_b128 v[174:177], v187
	ds_read_b128 v[178:181], v187 offset:1024
	ds_read_b128 v[182:185], v187 offset:2048
	ds_read_b128 v[190:193], v187 offset:3072
	v_cndmask_b32_e32 v2, v142, v143, vcc
	v_cndmask_b32_e32 v186, v140, v155, vcc
	v_cndmask_b32_e32 v137, v138, v156, vcc
	v_cndmask_b32_e32 v139, v136, v157, vcc
	v_lshl_add_u64 v[194:195], v[146:147], 0, s[56:57]
	s_add_i32 m0, s21, 0xc000
	ds_read_b128 v[212:215], v141
	ds_read_b128 v[216:219], v141 offset:1024
	ds_read_b128 v[224:227], v141 offset:2048
	ds_read_b128 v[228:231], v141 offset:3072
	ds_read_b128 v[232:235], v141 offset:4096
	ds_read_b128 v[236:239], v141 offset:5120
	ds_read_b128 v[240:243], v141 offset:6144
	ds_read_b128 v[244:247], v141 offset:7168
	global_load_lds_dwordx4 v[194:195], off
	v_lshl_add_u64 v[194:195], v[144:145], 0, s[56:57]
	s_add_i32 m0, s21, 0xe000
	s_nop 0
	global_load_lds_dwordx4 v[194:195], off
	s_waitcnt vmcnt(8)
	s_waitcnt lgkmcnt(0)
	s_barrier
	s_setprio 1
	s_waitcnt lgkmcnt(0)
	v_mfma_f32_16x16x32_bf16 v[128:131], v[158:161], v[212:215], v[128:131]
	v_mfma_f32_16x16x32_bf16 v[124:127], v[166:169], v[212:215], v[124:127]
	v_mfma_f32_16x16x32_bf16 v[112:115], v[158:161], v[224:227], v[112:115]
	v_mfma_f32_16x16x32_bf16 v[108:111], v[166:169], v[224:227], v[108:111]
	v_mfma_f32_16x16x32_bf16 v[96:99], v[158:161], v[232:235], v[96:99]
	v_mfma_f32_16x16x32_bf16 v[92:95], v[166:169], v[232:235], v[92:95]
	v_mfma_f32_16x16x32_bf16 v[80:83], v[158:161], v[240:243], v[80:83]
	v_mfma_f32_16x16x32_bf16 v[76:79], v[166:169], v[240:243], v[76:79]
	v_mfma_f32_16x16x32_bf16 v[128:131], v[162:165], v[216:219], v[128:131]
	v_mfma_f32_16x16x32_bf16 v[124:127], v[170:173], v[216:219], v[124:127]
	v_mfma_f32_16x16x32_bf16 v[112:115], v[162:165], v[228:231], v[112:115]
	v_mfma_f32_16x16x32_bf16 v[108:111], v[170:173], v[228:231], v[108:111]
	v_mfma_f32_16x16x32_bf16 v[96:99], v[162:165], v[236:239], v[96:99]
	v_mfma_f32_16x16x32_bf16 v[92:95], v[170:173], v[236:239], v[92:95]
	v_mfma_f32_16x16x32_bf16 v[80:83], v[162:165], v[244:247], v[80:83]
	v_mfma_f32_16x16x32_bf16 v[76:79], v[170:173], v[244:247], v[76:79]
	v_mfma_f32_16x16x32_bf16 v[120:123], v[174:177], v[212:215], v[120:123]
	v_mfma_f32_16x16x32_bf16 v[116:119], v[182:185], v[212:215], v[116:119]
	v_mfma_f32_16x16x32_bf16 v[104:107], v[174:177], v[224:227], v[104:107]
	v_mfma_f32_16x16x32_bf16 v[100:103], v[182:185], v[224:227], v[100:103]
	v_mfma_f32_16x16x32_bf16 v[88:91], v[174:177], v[232:235], v[88:91]
	v_mfma_f32_16x16x32_bf16 v[84:87], v[182:185], v[232:235], v[84:87]
	v_mfma_f32_16x16x32_bf16 v[72:75], v[174:177], v[240:243], v[72:75]
	v_mfma_f32_16x16x32_bf16 v[68:71], v[182:185], v[240:243], v[68:71]
	v_mfma_f32_16x16x32_bf16 v[120:123], v[178:181], v[216:219], v[120:123]
	v_mfma_f32_16x16x32_bf16 v[116:119], v[190:193], v[216:219], v[116:119]
	v_mfma_f32_16x16x32_bf16 v[104:107], v[178:181], v[228:231], v[104:107]
	v_mfma_f32_16x16x32_bf16 v[100:103], v[190:193], v[228:231], v[100:103]
	v_mfma_f32_16x16x32_bf16 v[88:91], v[178:181], v[236:239], v[88:91]
	v_mfma_f32_16x16x32_bf16 v[84:87], v[190:193], v[236:239], v[84:87]
	v_mfma_f32_16x16x32_bf16 v[72:75], v[178:181], v[244:247], v[72:75]
	v_mfma_f32_16x16x32_bf16 v[68:71], v[190:193], v[244:247], v[68:71]
	s_setprio 0
	s_barrier
	s_add_i32 s2, s2, s20
	v_lshl_add_u64 v[194:195], s[58:59], 0, v[134:135]
	s_mov_b32 m0, s2
	ds_read_b128 v[212:215], v141 offset:16384
	ds_read_b128 v[216:219], v141 offset:17408
	ds_read_b128 v[224:227], v141 offset:18432
	ds_read_b128 v[228:231], v141 offset:19456
	ds_read_b128 v[232:235], v141 offset:20480
	ds_read_b128 v[236:239], v141 offset:21504
	ds_read_b128 v[240:243], v141 offset:22528
	ds_read_b128 v[244:247], v141 offset:23552
	global_load_lds_dwordx4 v[194:195], off
	s_add_i32 m0, s2, 0x2000
	s_add_u32 s2, s58, 0x80000
	v_lshl_add_u64 v[248:249], s[58:59], 0, v[132:133]
	s_addc_u32 s3, s59, 0
	s_add_i32 s53, s53, s20
	global_load_lds_dwordx4 v[248:249], off
	v_lshl_add_u64 v[250:251], s[2:3], 0, v[134:135]
	s_mov_b32 m0, s53
	v_mov_b32_e32 v187, v3
	global_load_lds_dwordx4 v[250:251], off
	v_lshl_add_u64 v[250:251], s[2:3], 0, v[132:133]
	s_add_i32 m0, s53, 0x2000
	s_nop 0
	global_load_lds_dwordx4 v[250:251], off
	s_mov_b32 m0, s21
	v_lshl_add_u64 v[250:251], s[60:61], 0, v[2:3]
	global_load_lds_dwordx4 v2, s[60:61]
	s_mov_b32 m0, s22
	s_nop 0
	global_load_lds_dwordx4 v186, s[60:61]
	s_waitcnt vmcnt(8)
	s_waitcnt lgkmcnt(0)
	v_lshl_add_u64 v[186:187], s[60:61], 0, v[186:187]
	s_barrier
	s_setprio 1
	s_waitcnt lgkmcnt(0)
	s_cmp_eq_u32 s6, 8
	s_cbranch_scc1 .Lpadskip_p8_1
	v_mfma_f32_16x16x32_bf16 v[64:67], v[158:161], v[212:215], v[64:67]
	v_mfma_f32_16x16x32_bf16 v[56:59], v[166:169], v[212:215], v[56:59]
	v_mfma_f32_16x16x32_bf16 v[48:51], v[158:161], v[224:227], v[48:51]
	v_mfma_f32_16x16x32_bf16 v[40:43], v[166:169], v[224:227], v[40:43]
	v_mfma_f32_16x16x32_bf16 v[28:31], v[158:161], v[232:235], v[28:31]
	v_mfma_f32_16x16x32_bf16 v[20:23], v[166:169], v[232:235], v[20:23]
	v_mfma_f32_16x16x32_bf16 v[12:15], v[158:161], v[240:243], v[12:15]
	v_mfma_f32_16x16x32_bf16 v[4:7], v[166:169], v[240:243], v[4:7]
	v_mfma_f32_16x16x32_bf16 v[64:67], v[162:165], v[216:219], v[64:67]
	v_mfma_f32_16x16x32_bf16 v[56:59], v[170:173], v[216:219], v[56:59]
	v_mfma_f32_16x16x32_bf16 v[48:51], v[162:165], v[228:231], v[48:51]
	v_mfma_f32_16x16x32_bf16 v[40:43], v[170:173], v[228:231], v[40:43]
	v_mfma_f32_16x16x32_bf16 v[28:31], v[162:165], v[236:239], v[28:31]
	v_mfma_f32_16x16x32_bf16 v[20:23], v[170:173], v[236:239], v[20:23]
	v_mfma_f32_16x16x32_bf16 v[12:15], v[162:165], v[244:247], v[12:15]
	v_mfma_f32_16x16x32_bf16 v[4:7], v[170:173], v[244:247], v[4:7]
	v_mfma_f32_16x16x32_bf16 v[60:63], v[174:177], v[212:215], v[60:63]
	v_mfma_f32_16x16x32_bf16 v[52:55], v[182:185], v[212:215], v[52:55]
	v_mfma_f32_16x16x32_bf16 v[44:47], v[174:177], v[224:227], v[44:47]
	v_mfma_f32_16x16x32_bf16 v[32:35], v[182:185], v[224:227], v[32:35]
	v_mfma_f32_16x16x32_bf16 v[36:39], v[174:177], v[232:235], v[36:39]
	v_mfma_f32_16x16x32_bf16 v[24:27], v[182:185], v[232:235], v[24:27]
	v_mfma_f32_16x16x32_bf16 v[16:19], v[174:177], v[240:243], v[16:19]
	v_mfma_f32_16x16x32_bf16 v[8:11], v[182:185], v[240:243], v[8:11]
	v_mfma_f32_16x16x32_bf16 v[60:63], v[178:181], v[216:219], v[60:63]
	v_mfma_f32_16x16x32_bf16 v[52:55], v[190:193], v[216:219], v[52:55]
	v_mfma_f32_16x16x32_bf16 v[44:47], v[178:181], v[228:231], v[44:47]
	v_mfma_f32_16x16x32_bf16 v[32:35], v[190:193], v[228:231], v[32:35]
	v_mfma_f32_16x16x32_bf16 v[36:39], v[178:181], v[236:239], v[36:39]
	v_mfma_f32_16x16x32_bf16 v[24:27], v[190:193], v[236:239], v[24:27]
	v_mfma_f32_16x16x32_bf16 v[16:19], v[178:181], v[244:247], v[16:19]
	v_mfma_f32_16x16x32_bf16 v[8:11], v[190:193], v[244:247], v[8:11]
.Lpadskip_p8_1:
	s_setprio 0
	s_barrier
	s_add_i32 s2, 0, 0x18000
	v_add_u32_e32 v2, s2, v154
	s_add_i32 s53, 0, 0x1c000
	ds_read_b128 v[158:161], v2
	ds_read_b128 v[162:165], v2 offset:1024
	ds_read_b128 v[166:169], v2 offset:2048
	ds_read_b128 v[170:173], v2 offset:3072
	v_add_u32_e32 v2, s53, v154
	ds_read_b128 v[174:177], v2
	ds_read_b128 v[178:181], v2 offset:1024
	ds_read_b128 v[182:185], v2 offset:2048
	ds_read_b128 v[190:193], v2 offset:3072
	s_mov_b32 m0, s23
	ds_read_b128 v[212:215], v141 offset:32768
	ds_read_b128 v[216:219], v141 offset:33792
	ds_read_b128 v[224:227], v141 offset:34816
	ds_read_b128 v[228:231], v141 offset:35840
	ds_read_b128 v[232:235], v141 offset:36864
	ds_read_b128 v[236:239], v141 offset:37888
	ds_read_b128 v[240:243], v141 offset:38912
	ds_read_b128 v[244:247], v141 offset:39936
	global_load_lds_dwordx4 v137, s[60:61]
	s_mov_b32 m0, s24
	s_nop 0
	global_load_lds_dwordx4 v139, s[60:61]
	s_waitcnt vmcnt(8)
	s_waitcnt lgkmcnt(0)
	s_barrier
	s_setprio 1
	s_waitcnt lgkmcnt(0)
	v_mfma_f32_16x16x32_bf16 v[128:131], v[158:161], v[212:215], v[128:131]
	v_mfma_f32_16x16x32_bf16 v[124:127], v[166:169], v[212:215], v[124:127]
	v_mfma_f32_16x16x32_bf16 v[112:115], v[158:161], v[224:227], v[112:115]
	v_mfma_f32_16x16x32_bf16 v[108:111], v[166:169], v[224:227], v[108:111]
	v_mfma_f32_16x16x32_bf16 v[96:99], v[158:161], v[232:235], v[96:99]
	v_mfma_f32_16x16x32_bf16 v[92:95], v[166:169], v[232:235], v[92:95]
	v_mfma_f32_16x16x32_bf16 v[80:83], v[158:161], v[240:243], v[80:83]
	v_mfma_f32_16x16x32_bf16 v[76:79], v[166:169], v[240:243], v[76:79]
	v_mfma_f32_16x16x32_bf16 v[128:131], v[162:165], v[216:219], v[128:131]
	v_mfma_f32_16x16x32_bf16 v[124:127], v[170:173], v[216:219], v[124:127]
	v_mfma_f32_16x16x32_bf16 v[112:115], v[162:165], v[228:231], v[112:115]
	v_mfma_f32_16x16x32_bf16 v[108:111], v[170:173], v[228:231], v[108:111]
	v_mfma_f32_16x16x32_bf16 v[96:99], v[162:165], v[236:239], v[96:99]
	v_mfma_f32_16x16x32_bf16 v[92:95], v[170:173], v[236:239], v[92:95]
	v_mfma_f32_16x16x32_bf16 v[80:83], v[162:165], v[244:247], v[80:83]
	v_mfma_f32_16x16x32_bf16 v[76:79], v[170:173], v[244:247], v[76:79]
	v_mfma_f32_16x16x32_bf16 v[120:123], v[174:177], v[212:215], v[120:123]
	v_mfma_f32_16x16x32_bf16 v[116:119], v[182:185], v[212:215], v[116:119]
	v_mfma_f32_16x16x32_bf16 v[104:107], v[174:177], v[224:227], v[104:107]
	v_mfma_f32_16x16x32_bf16 v[100:103], v[182:185], v[224:227], v[100:103]
	v_mfma_f32_16x16x32_bf16 v[88:91], v[174:177], v[232:235], v[88:91]
	v_mfma_f32_16x16x32_bf16 v[84:87], v[182:185], v[232:235], v[84:87]
	v_mfma_f32_16x16x32_bf16 v[72:75], v[174:177], v[240:243], v[72:75]
	v_mfma_f32_16x16x32_bf16 v[68:71], v[182:185], v[240:243], v[68:71]
	v_mfma_f32_16x16x32_bf16 v[120:123], v[178:181], v[216:219], v[120:123]
	v_mfma_f32_16x16x32_bf16 v[116:119], v[190:193], v[216:219], v[116:119]
	v_mfma_f32_16x16x32_bf16 v[104:107], v[178:181], v[228:231], v[104:107]
	v_mfma_f32_16x16x32_bf16 v[100:103], v[190:193], v[228:231], v[100:103]
	v_mfma_f32_16x16x32_bf16 v[88:91], v[178:181], v[236:239], v[88:91]
	v_mfma_f32_16x16x32_bf16 v[84:87], v[190:193], v[236:239], v[84:87]
	v_mfma_f32_16x16x32_bf16 v[72:75], v[178:181], v[244:247], v[72:75]
	v_mfma_f32_16x16x32_bf16 v[68:71], v[190:193], v[244:247], v[68:71]
	s_setprio 0
	s_barrier
	s_add_i32 s2, s2, s20
	v_lshl_add_u64 v[194:195], v[194:195], 0, s[30:31]
	s_mov_b32 m0, s2
	ds_read_b128 v[212:215], v141 offset:49152
	ds_read_b128 v[216:219], v141 offset:50176
	ds_read_b128 v[224:227], v141 offset:51200
	ds_read_b128 v[228:231], v141 offset:52224
	ds_read_b128 v[232:235], v141 offset:53248
	ds_read_b128 v[236:239], v141 offset:54272
	ds_read_b128 v[240:243], v141 offset:55296
	ds_read_b128 v[244:247], v141 offset:56320
	global_load_lds_dwordx4 v[194:195], off
	s_add_i32 m0, s2, 0x2000
	s_add_u32 s2, s58, 0x80080
	v_lshl_add_u64 v[194:195], v[248:249], 0, s[30:31]
	s_addc_u32 s3, s59, 0
	s_add_i32 s53, s53, s20
	global_load_lds_dwordx4 v[194:195], off
	v_lshl_add_u64 v[194:195], s[2:3], 0, v[134:135]
	s_mov_b32 m0, s53
	v_lshl_add_u64 v[186:187], v[186:187], 0, s[30:31]
	global_load_lds_dwordx4 v[194:195], off
	v_lshl_add_u64 v[194:195], s[2:3], 0, v[132:133]
	s_add_i32 m0, s53, 0x2000
	s_nop 0
	global_load_lds_dwordx4 v[194:195], off
	v_lshl_add_u64 v[194:195], v[250:251], 0, s[30:31]
	s_mov_b32 m0, s26
	s_nop 0
	global_load_lds_dwordx4 v[194:195], off
	s_mov_b32 m0, s27
	s_nop 0
	global_load_lds_dwordx4 v[186:187], off
	s_waitcnt vmcnt(8)
	s_waitcnt lgkmcnt(0)
	s_barrier
	s_setprio 1
	s_waitcnt lgkmcnt(0)
	s_cmp_eq_u32 s6, 8
	s_cbranch_scc1 .Lpadskip_p8_3
	v_mfma_f32_16x16x32_bf16 v[64:67], v[158:161], v[212:215], v[64:67]
	v_mfma_f32_16x16x32_bf16 v[56:59], v[166:169], v[212:215], v[56:59]
	v_mfma_f32_16x16x32_bf16 v[48:51], v[158:161], v[224:227], v[48:51]
	v_mfma_f32_16x16x32_bf16 v[40:43], v[166:169], v[224:227], v[40:43]
	v_mfma_f32_16x16x32_bf16 v[28:31], v[158:161], v[232:235], v[28:31]
	v_mfma_f32_16x16x32_bf16 v[20:23], v[166:169], v[232:235], v[20:23]
	v_mfma_f32_16x16x32_bf16 v[12:15], v[158:161], v[240:243], v[12:15]
	v_mfma_f32_16x16x32_bf16 v[4:7], v[166:169], v[240:243], v[4:7]
	v_mfma_f32_16x16x32_bf16 v[64:67], v[162:165], v[216:219], v[64:67]
	v_mfma_f32_16x16x32_bf16 v[56:59], v[170:173], v[216:219], v[56:59]
	v_mfma_f32_16x16x32_bf16 v[48:51], v[162:165], v[228:231], v[48:51]
	v_mfma_f32_16x16x32_bf16 v[40:43], v[170:173], v[228:231], v[40:43]
	v_mfma_f32_16x16x32_bf16 v[28:31], v[162:165], v[236:239], v[28:31]
	v_mfma_f32_16x16x32_bf16 v[20:23], v[170:173], v[236:239], v[20:23]
	v_mfma_f32_16x16x32_bf16 v[12:15], v[162:165], v[244:247], v[12:15]
	v_mfma_f32_16x16x32_bf16 v[4:7], v[170:173], v[244:247], v[4:7]
	v_mfma_f32_16x16x32_bf16 v[60:63], v[174:177], v[212:215], v[60:63]
	v_mfma_f32_16x16x32_bf16 v[52:55], v[182:185], v[212:215], v[52:55]
	v_mfma_f32_16x16x32_bf16 v[44:47], v[174:177], v[224:227], v[44:47]
	v_mfma_f32_16x16x32_bf16 v[32:35], v[182:185], v[224:227], v[32:35]
	v_mfma_f32_16x16x32_bf16 v[36:39], v[174:177], v[232:235], v[36:39]
	v_mfma_f32_16x16x32_bf16 v[24:27], v[182:185], v[232:235], v[24:27]
	v_mfma_f32_16x16x32_bf16 v[16:19], v[174:177], v[240:243], v[16:19]
	v_mfma_f32_16x16x32_bf16 v[8:11], v[182:185], v[240:243], v[8:11]
	v_mfma_f32_16x16x32_bf16 v[60:63], v[178:181], v[216:219], v[60:63]
	v_mfma_f32_16x16x32_bf16 v[52:55], v[190:193], v[216:219], v[52:55]
	v_mfma_f32_16x16x32_bf16 v[44:47], v[178:181], v[228:231], v[44:47]
	v_mfma_f32_16x16x32_bf16 v[32:35], v[190:193], v[228:231], v[32:35]
	v_mfma_f32_16x16x32_bf16 v[36:39], v[178:181], v[236:239], v[36:39]
	v_mfma_f32_16x16x32_bf16 v[24:27], v[190:193], v[236:239], v[24:27]
	v_mfma_f32_16x16x32_bf16 v[16:19], v[178:181], v[244:247], v[16:19]
	v_mfma_f32_16x16x32_bf16 v[8:11], v[190:193], v[244:247], v[8:11]

.LBB0_2430:
	s_add_u32 s2, s56, 0x80
	s_addc_u32 s3, s57, 0
	s_cmp_eq_u32 s41, 28
	s_cselect_b32 s61, s51, s3
	s_cselect_b32 s60, s50, s2
	s_cselect_b32 s59, s55, s7
	s_cselect_b32 s58, s54, s6
	s_add_i32 s2, 0, 0x10000
	v_add_u32_e32 v146, s2, v150
	s_add_i32 s43, 0, 0x14000
	ds_read_b128 v[152:155], v146
	ds_read_b128 v[156:159], v146 offset:1024
	ds_read_b128 v[160:163], v146 offset:2048
	ds_read_b128 v[164:167], v146 offset:3072
	v_add_u32_e32 v146, s43, v150
	ds_read_b128 v[168:171], v146
	ds_read_b128 v[172:175], v146 offset:1024
	ds_read_b128 v[176:179], v146 offset:2048
	ds_read_b128 v[180:183], v146 offset:3072
	v_lshl_add_u64 v[146:147], s[56:57], 0, v[144:145]
	s_add_i32 m0, s23, 0xc000
	ds_read_b128 v[184:187], v151
	ds_read_b128 v[190:193], v151 offset:1024
	ds_read_b128 v[212:215], v151 offset:2048
	ds_read_b128 v[216:219], v151 offset:3072
	ds_read_b128 v[224:227], v151 offset:4096
	ds_read_b128 v[228:231], v151 offset:5120
	ds_read_b128 v[232:235], v151 offset:6144
	ds_read_b128 v[236:239], v151 offset:7168
	global_load_lds_dwordx4 v[146:147], off
	v_lshl_add_u64 v[146:147], s[56:57], 0, v[142:143]
	s_add_i32 m0, s23, 0xe000
	s_nop 0
	global_load_lds_dwordx4 v[146:147], off
	s_waitcnt vmcnt(8)
	s_waitcnt lgkmcnt(0)
	s_barrier
	s_setprio 1
	s_waitcnt lgkmcnt(0)
	v_mfma_f32_16x16x32_bf16 v[128:131], v[152:155], v[184:187], v[128:131]
	v_mfma_f32_16x16x32_bf16 v[124:127], v[160:163], v[184:187], v[124:127]
	v_mfma_f32_16x16x32_bf16 v[120:123], v[152:155], v[212:215], v[120:123]
	v_mfma_f32_16x16x32_bf16 v[116:119], v[160:163], v[212:215], v[116:119]
	v_mfma_f32_16x16x32_bf16 v[104:107], v[152:155], v[224:227], v[104:107]
	v_mfma_f32_16x16x32_bf16 v[100:103], v[160:163], v[224:227], v[100:103]
	v_mfma_f32_16x16x32_bf16 v[88:91], v[152:155], v[232:235], v[88:91]
	v_mfma_f32_16x16x32_bf16 v[84:87], v[160:163], v[232:235], v[84:87]
	v_mfma_f32_16x16x32_bf16 v[128:131], v[156:159], v[190:193], v[128:131]
	v_mfma_f32_16x16x32_bf16 v[124:127], v[164:167], v[190:193], v[124:127]
	v_mfma_f32_16x16x32_bf16 v[120:123], v[156:159], v[216:219], v[120:123]
	v_mfma_f32_16x16x32_bf16 v[116:119], v[164:167], v[216:219], v[116:119]
	v_mfma_f32_16x16x32_bf16 v[104:107], v[156:159], v[228:231], v[104:107]
	v_mfma_f32_16x16x32_bf16 v[100:103], v[164:167], v[228:231], v[100:103]
	v_mfma_f32_16x16x32_bf16 v[88:91], v[156:159], v[236:239], v[88:91]
	v_mfma_f32_16x16x32_bf16 v[84:87], v[164:167], v[236:239], v[84:87]
	v_mfma_f32_16x16x32_bf16 v[112:115], v[168:171], v[184:187], v[112:115]
	v_mfma_f32_16x16x32_bf16 v[108:111], v[176:179], v[184:187], v[108:111]
	v_mfma_f32_16x16x32_bf16 v[96:99], v[168:171], v[212:215], v[96:99]
	v_mfma_f32_16x16x32_bf16 v[92:95], v[176:179], v[212:215], v[92:95]
	v_mfma_f32_16x16x32_bf16 v[80:83], v[168:171], v[224:227], v[80:83]
	v_mfma_f32_16x16x32_bf16 v[72:75], v[176:179], v[224:227], v[72:75]
	v_mfma_f32_16x16x32_bf16 v[56:59], v[168:171], v[232:235], v[56:59]
	v_mfma_f32_16x16x32_bf16 v[52:55], v[176:179], v[232:235], v[52:55]
	v_mfma_f32_16x16x32_bf16 v[112:115], v[172:175], v[190:193], v[112:115]
	v_mfma_f32_16x16x32_bf16 v[108:111], v[180:183], v[190:193], v[108:111]
	v_mfma_f32_16x16x32_bf16 v[96:99], v[172:175], v[216:219], v[96:99]
	v_mfma_f32_16x16x32_bf16 v[92:95], v[180:183], v[216:219], v[92:95]
	v_mfma_f32_16x16x32_bf16 v[80:83], v[172:175], v[228:231], v[80:83]
	v_mfma_f32_16x16x32_bf16 v[72:75], v[180:183], v[228:231], v[72:75]
	v_mfma_f32_16x16x32_bf16 v[56:59], v[172:175], v[236:239], v[56:59]
	v_mfma_f32_16x16x32_bf16 v[52:55], v[180:183], v[236:239], v[52:55]
	s_setprio 0
	s_barrier
	s_add_i32 s2, s2, s21
	v_lshl_add_u64 v[146:147], s[58:59], 0, v[2:3]
	s_mov_b32 m0, s2
	ds_read_b128 v[184:187], v151 offset:16384
	ds_read_b128 v[190:193], v151 offset:17408
	ds_read_b128 v[212:215], v151 offset:18432
	ds_read_b128 v[216:219], v151 offset:19456
	ds_read_b128 v[224:227], v151 offset:20480
	ds_read_b128 v[228:231], v151 offset:21504
	ds_read_b128 v[232:235], v151 offset:22528
	ds_read_b128 v[236:239], v151 offset:23552
	global_load_lds_dwordx4 v[146:147], off
	s_add_i32 m0, s2, 0x2000
	s_add_u32 s2, s58, 0x80000
	v_lshl_add_u64 v[194:195], s[58:59], 0, v[132:133]
	s_addc_u32 s3, s59, 0
	s_add_i32 s43, s43, s21
	global_load_lds_dwordx4 v[194:195], off
	v_lshl_add_u64 v[240:241], s[2:3], 0, v[2:3]
	s_mov_b32 m0, s43
	v_lshl_add_u64 v[242:243], s[60:61], 0, v[136:137]
	global_load_lds_dwordx4 v[240:241], off
	v_lshl_add_u64 v[240:241], s[2:3], 0, v[132:133]
	s_add_i32 m0, s43, 0x2000
	s_nop 0
	global_load_lds_dwordx4 v[240:241], off
	v_lshl_add_u64 v[240:241], s[60:61], 0, v[134:135]
	s_mov_b32 m0, s23
	s_nop 0
	global_load_lds_dwordx4 v[240:241], off
	s_mov_b32 m0, s24
	s_nop 0
	global_load_lds_dwordx4 v[242:243], off
	s_waitcnt vmcnt(8)
	s_waitcnt lgkmcnt(0)
	s_barrier
	s_setprio 1
	s_waitcnt lgkmcnt(0)
	s_cmp_eq_u32 s36, 8
	s_cbranch_scc1 .Lpadskip_p9_1
	v_mfma_f32_16x16x32_bf16 v[36:39], v[152:155], v[184:187], v[36:39]
	v_mfma_f32_16x16x32_bf16 v[28:31], v[160:163], v[184:187], v[28:31]
	v_mfma_f32_16x16x32_bf16 v[24:27], v[152:155], v[212:215], v[24:27]
	v_mfma_f32_16x16x32_bf16 v[20:23], v[160:163], v[212:215], v[20:23]
	v_mfma_f32_16x16x32_bf16 v[16:19], v[152:155], v[224:227], v[16:19]
	v_mfma_f32_16x16x32_bf16 v[12:15], v[160:163], v[224:227], v[12:15]
	v_mfma_f32_16x16x32_bf16 v[8:11], v[152:155], v[232:235], v[8:11]
	v_mfma_f32_16x16x32_bf16 v[4:7], v[160:163], v[232:235], v[4:7]
	v_mfma_f32_16x16x32_bf16 v[36:39], v[156:159], v[190:193], v[36:39]
	v_mfma_f32_16x16x32_bf16 v[28:31], v[164:167], v[190:193], v[28:31]
	v_mfma_f32_16x16x32_bf16 v[24:27], v[156:159], v[216:219], v[24:27]
	v_mfma_f32_16x16x32_bf16 v[20:23], v[164:167], v[216:219], v[20:23]
	v_mfma_f32_16x16x32_bf16 v[16:19], v[156:159], v[228:231], v[16:19]
	v_mfma_f32_16x16x32_bf16 v[12:15], v[164:167], v[228:231], v[12:15]
	v_mfma_f32_16x16x32_bf16 v[8:11], v[156:159], v[236:239], v[8:11]
	v_mfma_f32_16x16x32_bf16 v[4:7], v[164:167], v[236:239], v[4:7]
	v_mfma_f32_16x16x32_bf16 v[68:71], v[168:171], v[184:187], v[68:71]
	v_mfma_f32_16x16x32_bf16 v[76:79], v[176:179], v[184:187], v[76:79]
	v_mfma_f32_16x16x32_bf16 v[60:63], v[168:171], v[212:215], v[60:63]
	v_mfma_f32_16x16x32_bf16 v[64:67], v[176:179], v[212:215], v[64:67]
	v_mfma_f32_16x16x32_bf16 v[44:47], v[168:171], v[224:227], v[44:47]
	v_mfma_f32_16x16x32_bf16 v[48:51], v[176:179], v[224:227], v[48:51]
	v_mfma_f32_16x16x32_bf16 v[32:35], v[168:171], v[232:235], v[32:35]
	v_mfma_f32_16x16x32_bf16 v[40:43], v[176:179], v[232:235], v[40:43]
	v_mfma_f32_16x16x32_bf16 v[68:71], v[172:175], v[190:193], v[68:71]
	v_mfma_f32_16x16x32_bf16 v[76:79], v[180:183], v[190:193], v[76:79]
	v_mfma_f32_16x16x32_bf16 v[60:63], v[172:175], v[216:219], v[60:63]
	v_mfma_f32_16x16x32_bf16 v[64:67], v[180:183], v[216:219], v[64:67]
	v_mfma_f32_16x16x32_bf16 v[44:47], v[172:175], v[228:231], v[44:47]
	v_mfma_f32_16x16x32_bf16 v[48:51], v[180:183], v[228:231], v[48:51]
	v_mfma_f32_16x16x32_bf16 v[32:35], v[172:175], v[236:239], v[32:35]
	v_mfma_f32_16x16x32_bf16 v[40:43], v[180:183], v[236:239], v[40:43]
.Lpadskip_p9_1:
	s_setprio 0
	s_barrier
	s_add_i32 s2, 0, 0x18000
	s_add_i32 s43, 0, 0x1c000
	v_add_u32_e32 v164, s2, v150
	v_add_u32_e32 v180, s43, v150
	ds_read_b128 v[152:155], v164
	ds_read_b128 v[156:159], v164 offset:1024
	ds_read_b128 v[160:163], v164 offset:2048
	ds_read_b128 v[164:167], v164 offset:3072
	ds_read_b128 v[168:171], v180
	ds_read_b128 v[172:175], v180 offset:1024
	ds_read_b128 v[176:179], v180 offset:2048
	ds_read_b128 v[180:183], v180 offset:3072
	s_mov_b32 m0, s25
	v_lshl_add_u64 v[244:245], s[60:61], 0, v[138:139]
	ds_read_b128 v[184:187], v151 offset:32768
	ds_read_b128 v[190:193], v151 offset:33792
	ds_read_b128 v[212:215], v151 offset:34816
	ds_read_b128 v[216:219], v151 offset:35840
	ds_read_b128 v[224:227], v151 offset:36864
	ds_read_b128 v[228:231], v151 offset:37888
	ds_read_b128 v[232:235], v151 offset:38912
	ds_read_b128 v[236:239], v151 offset:39936
	global_load_lds_dwordx4 v[244:245], off
	v_lshl_add_u64 v[244:245], s[60:61], 0, v[140:141]
	s_mov_b32 m0, s26
	s_nop 0
	global_load_lds_dwordx4 v[244:245], off
	s_waitcnt vmcnt(8)
	s_waitcnt lgkmcnt(0)
	s_barrier
	s_setprio 1
	s_waitcnt lgkmcnt(0)
	v_mfma_f32_16x16x32_bf16 v[128:131], v[152:155], v[184:187], v[128:131]
	v_mfma_f32_16x16x32_bf16 v[124:127], v[160:163], v[184:187], v[124:127]
	v_mfma_f32_16x16x32_bf16 v[120:123], v[152:155], v[212:215], v[120:123]
	v_mfma_f32_16x16x32_bf16 v[116:119], v[160:163], v[212:215], v[116:119]
	v_mfma_f32_16x16x32_bf16 v[104:107], v[152:155], v[224:227], v[104:107]
	v_mfma_f32_16x16x32_bf16 v[100:103], v[160:163], v[224:227], v[100:103]
	v_mfma_f32_16x16x32_bf16 v[88:91], v[152:155], v[232:235], v[88:91]
	v_mfma_f32_16x16x32_bf16 v[84:87], v[160:163], v[232:235], v[84:87]
	v_mfma_f32_16x16x32_bf16 v[128:131], v[156:159], v[190:193], v[128:131]
	v_mfma_f32_16x16x32_bf16 v[124:127], v[164:167], v[190:193], v[124:127]
	v_mfma_f32_16x16x32_bf16 v[120:123], v[156:159], v[216:219], v[120:123]
	v_mfma_f32_16x16x32_bf16 v[116:119], v[164:167], v[216:219], v[116:119]
	v_mfma_f32_16x16x32_bf16 v[104:107], v[156:159], v[228:231], v[104:107]
	v_mfma_f32_16x16x32_bf16 v[100:103], v[164:167], v[228:231], v[100:103]
	v_mfma_f32_16x16x32_bf16 v[88:91], v[156:159], v[236:239], v[88:91]
	v_mfma_f32_16x16x32_bf16 v[84:87], v[164:167], v[236:239], v[84:87]
	v_mfma_f32_16x16x32_bf16 v[112:115], v[168:171], v[184:187], v[112:115]
	v_mfma_f32_16x16x32_bf16 v[108:111], v[176:179], v[184:187], v[108:111]
	v_mfma_f32_16x16x32_bf16 v[96:99], v[168:171], v[212:215], v[96:99]
	v_mfma_f32_16x16x32_bf16 v[92:95], v[176:179], v[212:215], v[92:95]
	v_mfma_f32_16x16x32_bf16 v[80:83], v[168:171], v[224:227], v[80:83]
	v_mfma_f32_16x16x32_bf16 v[72:75], v[176:179], v[224:227], v[72:75]
	v_mfma_f32_16x16x32_bf16 v[56:59], v[168:171], v[232:235], v[56:59]
	v_mfma_f32_16x16x32_bf16 v[52:55], v[176:179], v[232:235], v[52:55]
	v_mfma_f32_16x16x32_bf16 v[112:115], v[172:175], v[190:193], v[112:115]
	v_mfma_f32_16x16x32_bf16 v[108:111], v[180:183], v[190:193], v[108:111]
	v_mfma_f32_16x16x32_bf16 v[96:99], v[172:175], v[216:219], v[96:99]
	v_mfma_f32_16x16x32_bf16 v[92:95], v[180:183], v[216:219], v[92:95]
	v_mfma_f32_16x16x32_bf16 v[80:83], v[172:175], v[228:231], v[80:83]
	v_mfma_f32_16x16x32_bf16 v[72:75], v[180:183], v[228:231], v[72:75]
	v_mfma_f32_16x16x32_bf16 v[56:59], v[172:175], v[236:239], v[56:59]
	v_mfma_f32_16x16x32_bf16 v[52:55], v[180:183], v[236:239], v[52:55]
	s_setprio 0
	s_barrier
	s_add_i32 s2, s2, s21
	v_lshl_add_u64 v[146:147], v[146:147], 0, s[30:31]
	s_mov_b32 m0, s2
	ds_read_b128 v[184:187], v151 offset:49152
	ds_read_b128 v[190:193], v151 offset:50176
	ds_read_b128 v[212:215], v151 offset:51200
	ds_read_b128 v[216:219], v151 offset:52224
	ds_read_b128 v[224:227], v151 offset:53248
	ds_read_b128 v[228:231], v151 offset:54272
	ds_read_b128 v[232:235], v151 offset:55296
	ds_read_b128 v[236:239], v151 offset:56320
	global_load_lds_dwordx4 v[146:147], off
	s_add_i32 m0, s2, 0x2000
	s_add_u32 s2, s58, 0x80080
	v_lshl_add_u64 v[146:147], v[194:195], 0, s[30:31]
	s_addc_u32 s3, s59, 0
	s_add_i32 s43, s43, s21
	global_load_lds_dwordx4 v[146:147], off
	v_lshl_add_u64 v[146:147], s[2:3], 0, v[2:3]
	s_mov_b32 m0, s43
	s_nop 0
	global_load_lds_dwordx4 v[146:147], off
	v_lshl_add_u64 v[146:147], s[2:3], 0, v[132:133]
	s_add_i32 m0, s43, 0x2000
	s_nop 0
	global_load_lds_dwordx4 v[146:147], off
	v_lshl_add_u64 v[146:147], v[240:241], 0, s[30:31]
	s_mov_b32 m0, s28
	s_nop 0
	global_load_lds_dwordx4 v[146:147], off
	v_lshl_add_u64 v[146:147], v[242:243], 0, s[30:31]
	s_mov_b32 m0, s29
	s_nop 0
	global_load_lds_dwordx4 v[146:147], off
	s_waitcnt vmcnt(8)
	s_waitcnt lgkmcnt(0)
	s_barrier
	s_setprio 1
	s_waitcnt lgkmcnt(0)
	s_cmp_eq_u32 s36, 8
	s_cbranch_scc1 .Lpadskip_p9_3
	v_mfma_f32_16x16x32_bf16 v[36:39], v[152:155], v[184:187], v[36:39]
	v_mfma_f32_16x16x32_bf16 v[28:31], v[160:163], v[184:187], v[28:31]
	v_mfma_f32_16x16x32_bf16 v[24:27], v[152:155], v[212:215], v[24:27]
	v_mfma_f32_16x16x32_bf16 v[20:23], v[160:163], v[212:215], v[20:23]
	v_mfma_f32_16x16x32_bf16 v[16:19], v[152:155], v[224:227], v[16:19]
	v_mfma_f32_16x16x32_bf16 v[12:15], v[160:163], v[224:227], v[12:15]
	v_mfma_f32_16x16x32_bf16 v[8:11], v[152:155], v[232:235], v[8:11]
	v_mfma_f32_16x16x32_bf16 v[4:7], v[160:163], v[232:235], v[4:7]
	v_mfma_f32_16x16x32_bf16 v[36:39], v[156:159], v[190:193], v[36:39]
	v_mfma_f32_16x16x32_bf16 v[28:31], v[164:167], v[190:193], v[28:31]
	v_mfma_f32_16x16x32_bf16 v[24:27], v[156:159], v[216:219], v[24:27]
	v_mfma_f32_16x16x32_bf16 v[20:23], v[164:167], v[216:219], v[20:23]
	v_mfma_f32_16x16x32_bf16 v[16:19], v[156:159], v[228:231], v[16:19]
	v_mfma_f32_16x16x32_bf16 v[12:15], v[164:167], v[228:231], v[12:15]
	v_mfma_f32_16x16x32_bf16 v[8:11], v[156:159], v[236:239], v[8:11]
	v_mfma_f32_16x16x32_bf16 v[4:7], v[164:167], v[236:239], v[4:7]
	v_mfma_f32_16x16x32_bf16 v[68:71], v[168:171], v[184:187], v[68:71]
	v_mfma_f32_16x16x32_bf16 v[76:79], v[176:179], v[184:187], v[76:79]
	v_mfma_f32_16x16x32_bf16 v[60:63], v[168:171], v[212:215], v[60:63]
	v_mfma_f32_16x16x32_bf16 v[64:67], v[176:179], v[212:215], v[64:67]
	v_mfma_f32_16x16x32_bf16 v[44:47], v[168:171], v[224:227], v[44:47]
	v_mfma_f32_16x16x32_bf16 v[48:51], v[176:179], v[224:227], v[48:51]
	v_mfma_f32_16x16x32_bf16 v[32:35], v[168:171], v[232:235], v[32:35]
	v_mfma_f32_16x16x32_bf16 v[40:43], v[176:179], v[232:235], v[40:43]
	v_mfma_f32_16x16x32_bf16 v[68:71], v[172:175], v[190:193], v[68:71]
	v_mfma_f32_16x16x32_bf16 v[76:79], v[180:183], v[190:193], v[76:79]
	v_mfma_f32_16x16x32_bf16 v[60:63], v[172:175], v[216:219], v[60:63]
	v_mfma_f32_16x16x32_bf16 v[64:67], v[180:183], v[216:219], v[64:67]
	v_mfma_f32_16x16x32_bf16 v[44:47], v[172:175], v[228:231], v[44:47]
	v_mfma_f32_16x16x32_bf16 v[48:51], v[180:183], v[228:231], v[48:51]
	v_mfma_f32_16x16x32_bf16 v[32:35], v[172:175], v[236:239], v[32:35]
	v_mfma_f32_16x16x32_bf16 v[40:43], v[180:183], v[236:239], v[40:43]
